# grouped-GEMM unit top: next-unit TILEE and row-index load results consumed at the K-loop exit instead of behind vmcnt(0) at the top (P8,P9); plus attention LDS read pipelining
# speedup vs baseline: 1.0070x; 1.0035x over previous
; #define PG8_VOFF(dst, U) do { if constexpr (GATHER) { _Pragma("unroll") for (int h = 0; h < 2; ++h) _Pragma("unroll") for (int i = 0; i < 2; ++i) { \
;         const int row = g.rowidx[(U).pm * BM + h * HALF + i * 64 + R0]; dst[h][i] = (unsigned)row * (unsigned)RB + (unsigned)C0 * 2u; } } } while (0)
; template <class Epi, bool GATHER, int MODE, bool SPLIT = false>
; __device__ __forceinline__ void gemm_phase(PG8_LAS unsigned char* lds, const Gemm g, const Order& S, const Epi& E) {
;     ...
;         float rs2[2] = {0.f, 0.f};
;         if constexpr (MODE == 2) {
; #pragma unroll
;             for (int a = 0; a < 2; ++a) rs2[a] = g.rowscale[cur.pm * BM + a * HALF + wr * 64 + fq * 16 + fr]; }
;         const bool has_next = S.next(ui + 1, nxt);
;         const char* nB = has_next ? (const char*)g.Bt + (size_t)nxt.e * g.bstride + (size_t)nxt.pn * tstep : cB;
;         const size_t nAr = has_next ? (size_t)nxt.pm * tstep : cAr;
;         if (has_next) { PG8_VOFF(nv, nxt); }
.LBB0_797:
	s_lshl_b32 s1, s10, 8
	v_add_u32_e32 v2, s1, v171
	v_ashrrev_i32_e32 v3, 31, v2
	v_lshl_add_u64 v[4:5], v[2:3], 2, s[14:15]
	v_add_u32_e32 v2, 0x80, v2
	v_ashrrev_i32_e32 v3, 31, v2
	v_lshl_add_u64 v[2:3], v[2:3], 2, s[14:15]
	global_load_dword v165, v[4:5], off
	global_load_dword v188, v[2:3], off
	s_add_i32 s47, s47, 1
	s_mul_i32 s2, s47, s64
	s_mul_hi_u32 s3, s47, s33
	s_add_i32 s3, s3, s2
	s_mul_i32 s2, s47, s33
	s_add_u32 s2, s2, s92
	s_addc_u32 s3, s3, s45
	v_cmp_ge_i64_e32 vcc, s[2:3], v[162:163]
	v_cmp_lt_i64_e64 s[4:5], s[2:3], v[162:163]
	s_cbranch_vccnz .LBB0_799
	s_ashr_i32 s3, s2, 31
	s_lshr_b32 s3, s3, 29
	s_add_i32 s3, s2, s3
	s_ashr_i32 s10, s3, 3
	s_and_b32 s3, s3, -8
	s_sub_i32 s2, s2, s3
	s_cmp_lt_i32 s2, 0
	s_cselect_b32 s3, s46, s44
	s_mul_i32 s2, s3, s2
	s_add_i32 s2, s2, s10
	s_ashr_i32 s3, s2, 31
	s_lshr_b32 s3, s3, 26
	s_add_i32 s3, s2, s3
	s_ashr_i32 s10, s3, 6
	s_lshl_b32 s10, s10, 2
	s_sub_i32 s11, s38, s10
	s_min_i32 s11, s11, 4
	s_abs_i32 s26, s11
	v_cvt_f32_u32_e32 v2, s26
	s_sub_i32 s28, 0, s26
	s_andn2_b32 s3, s3, 63
	s_sub_i32 s2, s2, s3
	v_rcp_iflag_f32_e32 v2, v2
	s_abs_i32 s3, s2
	s_xor_b32 s27, s2, s11
	s_ashr_i32 s27, s27, 31
	v_mul_f32_e32 v2, 0x4f7ffffe, v2
	v_cvt_u32_f32_e32 v2, v2
	s_nop 0
	v_readfirstlane_b32 s29, v2
	s_mul_i32 s28, s28, s29
	s_mul_hi_u32 s28, s29, s28
	s_add_i32 s29, s29, s28
	s_mul_hi_u32 s28, s3, s29
	s_mul_i32 s29, s28, s26
	s_sub_i32 s3, s3, s29
	s_add_i32 s30, s28, 1
	s_sub_i32 s29, s3, s26
	s_cmp_ge_u32 s3, s26
	s_cselect_b32 s28, s30, s28
	s_cselect_b32 s3, s29, s3
	s_add_i32 s29, s28, 1
	s_cmp_ge_u32 s3, s26
	s_cselect_b32 s3, s29, s28
	s_xor_b32 s3, s3, s27
	s_sub_i32 s26, s3, s27
	s_mul_i32 s3, s26, s11
	s_sub_i32 s2, s2, s3
	s_add_i32 s10, s2, s10
	s_ashr_i32 s11, s10, 31
	s_lshl_b64 s[2:3], s[10:11], 2
	s_add_u32 s2, s39, s2
	s_addc_u32 s3, s40, s3
	global_load_dword v230, v166, s[2:3]
.LBB0_799:
	s_nop 0
	v_cndmask_b32_e64 v2, 0, 1, s[4:5]
	v_cmp_ne_u32_e64 s[2:3], 1, v2
	s_andn2_b64 vcc, exec, s[4:5]
	v_mov_b32_e32 v184, v191
	v_mov_b32_e32 v185, v192
	v_mov_b32_e32 v186, v189
	v_mov_b32_e32 v187, v190
	s_cbranch_vccnz .LBB0_801
	v_lshl_add_u32 v2, s10, 8, v1
	v_ashrrev_i32_e32 v3, 31, v2
	v_lshl_add_u64 v[4:5], v[2:3], 2, s[8:9]
	v_add_u32_e32 v6, 64, v2
	v_add_u32_e32 v8, 0x80, v2
	v_add_u32_e32 v2, 0xc0, v2
	v_ashrrev_i32_e32 v7, 31, v6
	v_ashrrev_i32_e32 v3, 31, v2
	v_lshl_add_u64 v[6:7], v[6:7], 2, s[8:9]
	v_ashrrev_i32_e32 v9, 31, v8
	v_lshl_add_u64 v[2:3], v[2:3], 2, s[8:9]
	v_lshl_add_u64 v[8:9], v[8:9], 2, s[8:9]
	global_load_dword v231, v[4:5], off
	s_nop 0
	global_load_dword v232, v[6:7], off
	s_nop 0
	global_load_dword v233, v[8:9], off
	s_nop 0
	global_load_dword v234, v[2:3], off

; #define PG8_STAGEB(bufoff, gbase) glds2(voffB, (gbase), voffB, (gbase) + qstep, ldsb + (bufoff))
; #define PG8_STAGEA(bufoff, rowb, v, h, kb) do { if constexpr (GATHER) glds2((v)[h][0], Ab + (kb), (v)[h][1], Ab + (kb), ldsb + (bufoff)); \
;         else glds2(voffA, Ab + (rowb) + (h) * hstep + (kb), voffA, Ab + (rowb) + (h) * hstep + qstep + (kb), ldsb + (bufoff)); } while (0)
; #define PG8_LDA(dst, b, h) do { _Pragma("unroll") for (int m = 0; m < 4; ++m) _Pragma("unroll") for (int k = 0; k < 2; ++k) dst[m][k] = *(const PG8_LAS bf16x8*)(lds + PG8_SA(b, h) + aoff + m * 2048 + k * 1024); } while (0)
; #define PG8_LDB(dst, b, h) do { _Pragma("unroll") for (int n = 0; n < 2; ++n) _Pragma("unroll") for (int k = 0; k < 2; ++k) dst[n][k] = *(const PG8_LAS bf16x8*)(lds + PG8_SB(b, h) + boff + n * 2048 + k * 1024); } while (0)
; #define PG8_WAIT_V(n) asm volatile("s_waitcnt vmcnt(" #n ")" ::: "memory")
; #define PG8_WAIT_L(n) asm volatile("s_waitcnt lgkmcnt(" #n ")" ::: "memory")
; #define PG8_BAR __builtin_amdgcn_s_barrier()
; #define PG8_SCHED __builtin_amdgcn_sched_barrier(0)
; template <class Epi, bool GATHER, int MODE, bool SPLIT = false>
; __device__ __forceinline__ void gemm_phase(PG8_LAS unsigned char* lds, const Gemm g, const Order& S, const Epi& E) {
;     ...
;             PG8_LDB(B0, 0, 0); PG8_LDB(B1, 0, 1); PG8_SCHED; PG8_LDA(At, 0, 0); PG8_STAGEA(PG8_SA(1, 1), cAr, cv, 1, k1);
;             PG8_WAIT_V(8); PG8_WAIT_L(0); PG8_BAR; PG8_MMA(0, 0, At, B0); PG8_MMA(0, 1, At, B1); PG8_BAR; PG8_SCHED;
;             PG8_LDA(At, 0, 1); PG8_STAGEB(PG8_SB(0, 0), b2); PG8_STAGEB(PG8_SB(0, 1), b2 + hstep); PG8_STAGEA(PG8_SA(0, 0), cAr, cv, 0, k2);
.LBB0_802:
	ds_read_b128 v[158:161], v179
	ds_read_b128 v[150:153], v179 offset:1024
	ds_read_b128 v[154:157], v179 offset:2048
	ds_read_b128 v[146:149], v179 offset:3072
	ds_read_b128 v[142:145], v180
	ds_read_b128 v[130:133], v180 offset:1024
	ds_read_b128 v[138:141], v180 offset:2048
	ds_read_b128 v[134:137], v180 offset:3072
	s_add_u32 s66, s34, s30
	s_addc_u32 s67, s35, s31
	s_add_u32 s36, s66, 0x100
	s_addc_u32 s37, s67, 0
	ds_read_b128 v[194:197], v181
	ds_read_b128 v[198:201], v181 offset:1024
	ds_read_b128 v[202:205], v181 offset:2048
	ds_read_b128 v[206:209], v181 offset:3072
	ds_read_b128 v[210:213], v181 offset:4096
	ds_read_b128 v[214:217], v181 offset:5120
	ds_read_b128 v[218:221], v181 offset:6144
	ds_read_b128 v[222:225], v181 offset:7168
	s_add_u32 s27, s6, s30
	s_addc_u32 s29, s7, s31
	s_add_u32 s68, s27, 0x80
	s_addc_u32 s69, s29, 0
	s_mov_b32 s70, m0
	s_mov_b32 m0, s62
	s_nop 0
	global_load_lds_dwordx4 v189, s[68:69]
	s_mov_b32 m0, s63
	s_nop 0
	global_load_lds_dwordx4 v190, s[68:69]
	s_mov_b32 m0, s70
	s_waitcnt vmcnt(8)
	s_waitcnt lgkmcnt(0)
	s_barrier
	s_setprio 1
	s_waitcnt lgkmcnt(7)
	v_mfma_i32_16x16x64_i8 v[126:129], v[158:161], v[194:197], v[126:129]
	v_mfma_i32_16x16x64_i8 v[122:125], v[154:157], v[194:197], v[122:125]
	s_waitcnt lgkmcnt(5)
	v_mfma_i32_16x16x64_i8 v[118:121], v[158:161], v[202:205], v[118:121]
	v_mfma_i32_16x16x64_i8 v[106:109], v[154:157], v[202:205], v[106:109]
	s_waitcnt lgkmcnt(3)
	v_mfma_i32_16x16x64_i8 v[102:105], v[158:161], v[210:213], v[102:105]
	v_mfma_i32_16x16x64_i8 v[90:93], v[154:157], v[210:213], v[90:93]
	s_waitcnt lgkmcnt(1)
	v_mfma_i32_16x16x64_i8 v[86:89], v[158:161], v[218:221], v[86:89]
	v_mfma_i32_16x16x64_i8 v[74:77], v[154:157], v[218:221], v[74:77]
	v_mfma_i32_16x16x64_i8 v[126:129], v[150:153], v[198:201], v[126:129]
	v_mfma_i32_16x16x64_i8 v[122:125], v[146:149], v[198:201], v[122:125]
	v_mfma_i32_16x16x64_i8 v[118:121], v[150:153], v[206:209], v[118:121]
	v_mfma_i32_16x16x64_i8 v[106:109], v[146:149], v[206:209], v[106:109]
	v_mfma_i32_16x16x64_i8 v[102:105], v[150:153], v[214:217], v[102:105]
	v_mfma_i32_16x16x64_i8 v[90:93], v[146:149], v[214:217], v[90:93]
	s_waitcnt lgkmcnt(0)
	v_mfma_i32_16x16x64_i8 v[86:89], v[150:153], v[222:225], v[86:89]
	v_mfma_i32_16x16x64_i8 v[74:77], v[146:149], v[222:225], v[74:77]
	s_setprio 0
	s_setprio 1
	v_mfma_i32_16x16x64_i8 v[114:117], v[142:145], v[194:197], v[114:117]
	v_mfma_i32_16x16x64_i8 v[110:113], v[138:141], v[194:197], v[110:113]
	v_mfma_i32_16x16x64_i8 v[98:101], v[142:145], v[202:205], v[98:101]
	v_mfma_i32_16x16x64_i8 v[94:97], v[138:141], v[202:205], v[94:97]
	v_mfma_i32_16x16x64_i8 v[82:85], v[142:145], v[210:213], v[82:85]
	v_mfma_i32_16x16x64_i8 v[78:81], v[138:141], v[210:213], v[78:81]
	v_mfma_i32_16x16x64_i8 v[70:73], v[142:145], v[218:221], v[70:73]
	v_mfma_i32_16x16x64_i8 v[66:69], v[138:141], v[218:221], v[66:69]
	s_nop 0
	v_mfma_i32_16x16x64_i8 v[114:117], v[130:133], v[198:201], v[114:117]
	v_mfma_i32_16x16x64_i8 v[110:113], v[134:137], v[198:201], v[110:113]
	v_mfma_i32_16x16x64_i8 v[98:101], v[130:133], v[206:209], v[98:101]
	v_mfma_i32_16x16x64_i8 v[94:97], v[134:137], v[206:209], v[94:97]
	v_mfma_i32_16x16x64_i8 v[82:85], v[130:133], v[214:217], v[82:85]
	v_mfma_i32_16x16x64_i8 v[78:81], v[134:137], v[214:217], v[78:81]
	v_mfma_i32_16x16x64_i8 v[70:73], v[130:133], v[222:225], v[70:73]
	v_mfma_i32_16x16x64_i8 v[66:69], v[134:137], v[222:225], v[66:69]
	s_setprio 0
	s_barrier
	s_add_u32 s68, s66, 0x20100
	s_addc_u32 s69, s67, 0
	ds_read_b128 v[194:197], v181 offset:16384
	ds_read_b128 v[198:201], v181 offset:17408
	ds_read_b128 v[202:205], v181 offset:18432
	ds_read_b128 v[206:209], v181 offset:19456
	ds_read_b128 v[210:213], v181 offset:20480
	ds_read_b128 v[214:217], v181 offset:21504
	ds_read_b128 v[218:221], v181 offset:22528
	ds_read_b128 v[222:225], v181 offset:23552
	s_mov_b32 s70, m0
	s_mov_b32 m0, s49
	s_nop 0
	global_load_lds_dwordx4 v168, s[36:37]
	s_mov_b32 m0, s50
	s_nop 0
	global_load_lds_dwordx4 v168, s[68:69]
	s_mov_b32 m0, s70
	s_add_u32 s36, s66, 0x40100
	s_addc_u32 s37, s67, 0
	s_add_u32 s68, s66, 0x60100
	s_addc_u32 s69, s67, 0
	s_mov_b32 s70, m0
	s_mov_b32 m0, s51
	s_nop 0
	global_load_lds_dwordx4 v168, s[36:37]
	s_mov_b32 m0, s52
	s_nop 0
	global_load_lds_dwordx4 v168, s[68:69]
	s_mov_b32 m0, s70
	s_add_u32 s36, s27, 0x100
	s_addc_u32 s37, s29, 0
	s_mov_b32 s68, m0
	s_mov_b32 m0, s43
	s_nop 0
	global_load_lds_dwordx4 v191, s[36:37]
	s_mov_b32 m0, s53
	s_nop 0
	global_load_lds_dwordx4 v192, s[36:37]
	s_mov_b32 m0, s68
	s_waitcnt vmcnt(8)
	s_waitcnt lgkmcnt(0)
	s_barrier
; #define PG8_STAGEA(bufoff, rowb, v, h, kb) do { if constexpr (GATHER) glds2((v)[h][0], Ab + (kb), (v)[h][1], Ab + (kb), ldsb + (bufoff)); \
;         else glds2(voffA, Ab + (rowb) + (h) * hstep + (kb), voffA, Ab + (rowb) + (h) * hstep + qstep + (kb), ldsb + (bufoff)); } while (0)
; #define PG8_LDA(dst, b, h) do { _Pragma("unroll") for (int m = 0; m < 4; ++m) _Pragma("unroll") for (int k = 0; k < 2; ++k) dst[m][k] = *(const PG8_LAS bf16x8*)(lds + PG8_SA(b, h) + aoff + m * 2048 + k * 1024); } while (0)
; #define PG8_LDB(dst, b, h) do { _Pragma("unroll") for (int n = 0; n < 2; ++n) _Pragma("unroll") for (int k = 0; k < 2; ++k) dst[n][k] = *(const PG8_LAS bf16x8*)(lds + PG8_SB(b, h) + boff + n * 2048 + k * 1024); } while (0)
; #define PG8_WAIT_V(n) asm volatile("s_waitcnt vmcnt(" #n ")" ::: "memory")
; #define PG8_WAIT_L(n) asm volatile("s_waitcnt lgkmcnt(" #n ")" ::: "memory")
; #define PG8_BAR __builtin_amdgcn_s_barrier()
; #define PG8_SCHED __builtin_amdgcn_sched_barrier(0)
; template <class Epi, bool GATHER, int MODE, bool SPLIT = false>
; __device__ __forceinline__ void gemm_phase(PG8_LAS unsigned char* lds, const Gemm g, const Order& S, const Epi& E) {
;     ...
;             PG8_WAIT_V(8); PG8_WAIT_L(0); PG8_BAR; PG8_MMA(1, 0, At, B0); PG8_MMA(1, 1, At, B1); PG8_BAR; PG8_SCHED;
;             PG8_LDB(B0, 1, 0); PG8_LDB(B1, 1, 1); PG8_SCHED; PG8_LDA(At, 1, 0); PG8_STAGEA(PG8_SA(0, 1), cAr, cv, 1, k2);
;             PG8_WAIT_V(8); PG8_WAIT_L(0); PG8_BAR; PG8_MMA(0, 0, At, B0); PG8_MMA(0, 1, At, B1); PG8_BAR; PG8_SCHED;
	s_setprio 1
	s_waitcnt lgkmcnt(7)
	v_mfma_i32_16x16x64_i8 v[62:65], v[158:161], v[194:197], v[62:65]
	v_mfma_i32_16x16x64_i8 v[58:61], v[154:157], v[194:197], v[58:61]
	s_waitcnt lgkmcnt(5)
	v_mfma_i32_16x16x64_i8 v[46:49], v[158:161], v[202:205], v[46:49]
	v_mfma_i32_16x16x64_i8 v[42:45], v[154:157], v[202:205], v[42:45]
	s_waitcnt lgkmcnt(3)
	v_mfma_i32_16x16x64_i8 v[38:41], v[158:161], v[210:213], v[38:41]
	v_mfma_i32_16x16x64_i8 v[34:37], v[154:157], v[210:213], v[34:37]
	s_waitcnt lgkmcnt(1)
	v_mfma_i32_16x16x64_i8 v[22:25], v[158:161], v[218:221], v[22:25]
	v_mfma_i32_16x16x64_i8 v[18:21], v[154:157], v[218:221], v[18:21]
	v_mfma_i32_16x16x64_i8 v[62:65], v[150:153], v[198:201], v[62:65]
	v_mfma_i32_16x16x64_i8 v[58:61], v[146:149], v[198:201], v[58:61]
	v_mfma_i32_16x16x64_i8 v[46:49], v[150:153], v[206:209], v[46:49]
	v_mfma_i32_16x16x64_i8 v[42:45], v[146:149], v[206:209], v[42:45]
	v_mfma_i32_16x16x64_i8 v[38:41], v[150:153], v[214:217], v[38:41]
	v_mfma_i32_16x16x64_i8 v[34:37], v[146:149], v[214:217], v[34:37]
	s_waitcnt lgkmcnt(0)
	v_mfma_i32_16x16x64_i8 v[22:25], v[150:153], v[222:225], v[22:25]
	v_mfma_i32_16x16x64_i8 v[18:21], v[146:149], v[222:225], v[18:21]
	s_setprio 0
	s_setprio 1
	v_mfma_i32_16x16x64_i8 v[54:57], v[142:145], v[194:197], v[54:57]
	v_mfma_i32_16x16x64_i8 v[50:53], v[138:141], v[194:197], v[50:53]
	v_mfma_i32_16x16x64_i8 v[30:33], v[142:145], v[202:205], v[30:33]
	v_mfma_i32_16x16x64_i8 v[26:29], v[138:141], v[202:205], v[26:29]
	v_mfma_i32_16x16x64_i8 v[14:17], v[142:145], v[210:213], v[14:17]
	v_mfma_i32_16x16x64_i8 v[10:13], v[138:141], v[210:213], v[10:13]
	v_mfma_i32_16x16x64_i8 v[6:9], v[142:145], v[218:221], v[6:9]
	v_mfma_i32_16x16x64_i8 v[2:5], v[138:141], v[218:221], v[2:5]
	s_nop 0
	v_mfma_i32_16x16x64_i8 v[54:57], v[130:133], v[198:201], v[54:57]
	v_mfma_i32_16x16x64_i8 v[50:53], v[134:137], v[198:201], v[50:53]
	v_mfma_i32_16x16x64_i8 v[30:33], v[130:133], v[206:209], v[30:33]
	v_mfma_i32_16x16x64_i8 v[26:29], v[134:137], v[206:209], v[26:29]
	v_mfma_i32_16x16x64_i8 v[14:17], v[130:133], v[214:217], v[14:17]
	v_mfma_i32_16x16x64_i8 v[10:13], v[134:137], v[214:217], v[10:13]
	v_mfma_i32_16x16x64_i8 v[6:9], v[130:133], v[222:225], v[6:9]
	v_mfma_i32_16x16x64_i8 v[2:5], v[134:137], v[222:225], v[2:5]
	s_setprio 0
	s_barrier
	v_add_u32_e32 v138, 0x1c000, v178
	ds_read_b128 v[130:133], v182
	ds_read_b128 v[134:137], v182 offset:1024
	ds_read_b128 v[140:143], v182 offset:2048
	ds_read_b128 v[144:147], v182 offset:3072
	ds_read_b128 v[148:151], v138
	ds_read_b128 v[152:155], v138 offset:1024
	ds_read_b128 v[156:159], v138 offset:2048
	ds_read_b128 v[194:197], v138 offset:3072
	ds_read_b128 v[198:201], v181 offset:32768
	ds_read_b128 v[202:205], v181 offset:33792
	ds_read_b128 v[206:209], v181 offset:34816
	ds_read_b128 v[210:213], v181 offset:35840
	ds_read_b128 v[214:217], v181 offset:36864
	ds_read_b128 v[218:221], v181 offset:37888
	ds_read_b128 v[222:225], v181 offset:38912
	ds_read_b128 v[226:229], v181 offset:39936
	s_mov_b32 s68, m0
	s_mov_b32 m0, s54
	s_nop 0
	global_load_lds_dwordx4 v189, s[36:37]
	s_mov_b32 m0, s55
	s_nop 0
	global_load_lds_dwordx4 v190, s[36:37]
	s_mov_b32 m0, s68
	s_waitcnt vmcnt(8)
	s_waitcnt lgkmcnt(0)
	s_barrier
	s_setprio 1
	s_waitcnt lgkmcnt(7)
	v_mfma_i32_16x16x64_i8 v[126:129], v[130:133], v[198:201], v[126:129]
	v_mfma_i32_16x16x64_i8 v[122:125], v[140:143], v[198:201], v[122:125]
	s_waitcnt lgkmcnt(5)
	v_mfma_i32_16x16x64_i8 v[118:121], v[130:133], v[206:209], v[118:121]
	v_mfma_i32_16x16x64_i8 v[106:109], v[140:143], v[206:209], v[106:109]
	s_waitcnt lgkmcnt(3)
	v_mfma_i32_16x16x64_i8 v[102:105], v[130:133], v[214:217], v[102:105]
	v_mfma_i32_16x16x64_i8 v[90:93], v[140:143], v[214:217], v[90:93]
	s_waitcnt lgkmcnt(1)
	v_mfma_i32_16x16x64_i8 v[86:89], v[130:133], v[222:225], v[86:89]
	v_mfma_i32_16x16x64_i8 v[74:77], v[140:143], v[222:225], v[74:77]
	v_mfma_i32_16x16x64_i8 v[126:129], v[134:137], v[202:205], v[126:129]
	v_mfma_i32_16x16x64_i8 v[122:125], v[144:147], v[202:205], v[122:125]
	v_mfma_i32_16x16x64_i8 v[118:121], v[134:137], v[210:213], v[118:121]
	v_mfma_i32_16x16x64_i8 v[106:109], v[144:147], v[210:213], v[106:109]
	v_mfma_i32_16x16x64_i8 v[102:105], v[134:137], v[218:221], v[102:105]
	v_mfma_i32_16x16x64_i8 v[90:93], v[144:147], v[218:221], v[90:93]
	s_waitcnt lgkmcnt(0)
	v_mfma_i32_16x16x64_i8 v[86:89], v[134:137], v[226:229], v[86:89]
	v_mfma_i32_16x16x64_i8 v[74:77], v[144:147], v[226:229], v[74:77]
	s_setprio 0
	s_setprio 1
	v_mfma_i32_16x16x64_i8 v[114:117], v[148:151], v[198:201], v[114:117]
	v_mfma_i32_16x16x64_i8 v[110:113], v[156:159], v[198:201], v[110:113]
	v_mfma_i32_16x16x64_i8 v[98:101], v[148:151], v[206:209], v[98:101]
	v_mfma_i32_16x16x64_i8 v[94:97], v[156:159], v[206:209], v[94:97]
	v_mfma_i32_16x16x64_i8 v[82:85], v[148:151], v[214:217], v[82:85]
	v_mfma_i32_16x16x64_i8 v[78:81], v[156:159], v[214:217], v[78:81]
	v_mfma_i32_16x16x64_i8 v[70:73], v[148:151], v[222:225], v[70:73]
	v_mfma_i32_16x16x64_i8 v[66:69], v[156:159], v[222:225], v[66:69]
	s_nop 0
	v_mfma_i32_16x16x64_i8 v[114:117], v[152:155], v[202:205], v[114:117]
	v_mfma_i32_16x16x64_i8 v[110:113], v[194:197], v[202:205], v[110:113]
	v_mfma_i32_16x16x64_i8 v[98:101], v[152:155], v[210:213], v[98:101]
	v_mfma_i32_16x16x64_i8 v[94:97], v[194:197], v[210:213], v[94:97]
	v_mfma_i32_16x16x64_i8 v[82:85], v[152:155], v[218:221], v[82:85]
	v_mfma_i32_16x16x64_i8 v[78:81], v[194:197], v[218:221], v[78:81]
	v_mfma_i32_16x16x64_i8 v[70:73], v[152:155], v[226:229], v[70:73]
	v_mfma_i32_16x16x64_i8 v[66:69], v[194:197], v[226:229], v[66:69]
	s_setprio 0
	s_barrier
; #define PG8_STAGEB(bufoff, gbase) glds2(voffB, (gbase), voffB, (gbase) + qstep, ldsb + (bufoff))
; #define PG8_STAGEA(bufoff, rowb, v, h, kb) do { if constexpr (GATHER) glds2((v)[h][0], Ab + (kb), (v)[h][1], Ab + (kb), ldsb + (bufoff)); \
;         else glds2(voffA, Ab + (rowb) + (h) * hstep + (kb), voffA, Ab + (rowb) + (h) * hstep + qstep + (kb), ldsb + (bufoff)); } while (0)
; #define PG8_LDA(dst, b, h) do { _Pragma("unroll") for (int m = 0; m < 4; ++m) _Pragma("unroll") for (int k = 0; k < 2; ++k) dst[m][k] = *(const PG8_LAS bf16x8*)(lds + PG8_SA(b, h) + aoff + m * 2048 + k * 1024); } while (0)
; #define PG8_LDB(dst, b, h) do { _Pragma("unroll") for (int n = 0; n < 2; ++n) _Pragma("unroll") for (int k = 0; k < 2; ++k) dst[n][k] = *(const PG8_LAS bf16x8*)(lds + PG8_SB(b, h) + boff + n * 2048 + k * 1024); } while (0)
; #define PG8_WAIT_V(n) asm volatile("s_waitcnt vmcnt(" #n ")" ::: "memory")
; #define PG8_WAIT_L(n) asm volatile("s_waitcnt lgkmcnt(" #n ")" ::: "memory")
; #define PG8_BAR __builtin_amdgcn_s_barrier()
; #define PG8_SCHED __builtin_amdgcn_sched_barrier(0)
; #define PG8_VOFF(dst, U) do { if constexpr (GATHER) { _Pragma("unroll") for (int h = 0; h < 2; ++h) _Pragma("unroll") for (int i = 0; i < 2; ++i) { \
;         const int row = g.rowidx[(U).pm * BM + h * HALF + i * 64 + R0]; dst[h][i] = (unsigned)row * (unsigned)RB + (unsigned)C0 * 2u; } } } while (0)
; template <class Epi, bool GATHER, int MODE, bool SPLIT = false>
; __device__ __forceinline__ void gemm_phase(PG8_LAS unsigned char* lds, const Gemm g, const Order& S, const Epi& E) {
;     ...
;         const bool has_next = S.next(ui + 1, nxt);
;         const char* nB = has_next ? (const char*)g.Bt + (size_t)nxt.e * g.bstride + (size_t)nxt.pn * tstep : cB;
;         const size_t nAr = has_next ? (size_t)nxt.pm * tstep : cAr;
;         if (has_next) { PG8_VOFF(nv, nxt); }
;     ...
;             PG8_LDA(At, 1, 1); PG8_STAGEB(PG8_SB(1, 0), b3); PG8_STAGEB(PG8_SB(1, 1), b3 + hstep); PG8_STAGEA(PG8_SA(1, 0), cAr, cv, 0, k3);
;             PG8_WAIT_V(8); PG8_WAIT_L(0); PG8_BAR; PG8_MMA(1, 0, At, B0); PG8_MMA(1, 1, At, B1); PG8_BAR; PG8_SCHED;
;         }
;         {
;             const size_t k1 = (size_t)(nt - 1) * kstep;
;             PG8_LDB(B0, 0, 0); PG8_LDB(B1, 0, 1); PG8_SCHED; PG8_LDA(At, 0, 0); PG8_STAGEA(PG8_SA(1, 1), cAr, cv, 1, k1);
	s_add_u32 s36, s66, 0x180
	s_addc_u32 s37, s67, 0
	s_add_u32 s68, s66, 0x20180
	s_addc_u32 s69, s67, 0
	ds_read_b128 v[198:201], v181 offset:49152
	ds_read_b128 v[202:205], v181 offset:50176
	ds_read_b128 v[206:209], v181 offset:51200
	ds_read_b128 v[210:213], v181 offset:52224
	ds_read_b128 v[214:217], v181 offset:53248
	ds_read_b128 v[218:221], v181 offset:54272
	ds_read_b128 v[222:225], v181 offset:55296
	ds_read_b128 v[226:229], v181 offset:56320
	s_mov_b32 s70, m0
	s_mov_b32 m0, s56
	s_nop 0
	global_load_lds_dwordx4 v168, s[36:37]
	s_mov_b32 m0, s57
	s_nop 0
	global_load_lds_dwordx4 v168, s[68:69]
	s_mov_b32 m0, s70
	s_add_u32 s36, s66, 0x40180
	s_addc_u32 s37, s67, 0
	s_add_u32 s66, s66, 0x60180
	s_addc_u32 s67, s67, 0
	s_mov_b32 s68, m0
	s_mov_b32 m0, s60
	s_nop 0
	global_load_lds_dwordx4 v168, s[36:37]
	s_mov_b32 m0, s61
	s_nop 0
	global_load_lds_dwordx4 v168, s[66:67]
	s_mov_b32 m0, s68
	s_add_u32 s36, s27, 0x180
	s_addc_u32 s37, s29, 0
	s_mov_b32 s27, m0
	s_mov_b32 m0, s58
	s_nop 0
	global_load_lds_dwordx4 v191, s[36:37]
	s_mov_b32 m0, s59
	s_nop 0
	global_load_lds_dwordx4 v192, s[36:37]
	s_mov_b32 m0, s27
	s_waitcnt vmcnt(8)
	s_waitcnt lgkmcnt(0)
	s_barrier
	s_setprio 1
	s_waitcnt lgkmcnt(7)
	v_mfma_i32_16x16x64_i8 v[62:65], v[130:133], v[198:201], v[62:65]
	v_mfma_i32_16x16x64_i8 v[58:61], v[140:143], v[198:201], v[58:61]
	s_waitcnt lgkmcnt(5)
	v_mfma_i32_16x16x64_i8 v[46:49], v[130:133], v[206:209], v[46:49]
	v_mfma_i32_16x16x64_i8 v[42:45], v[140:143], v[206:209], v[42:45]
	s_waitcnt lgkmcnt(3)
	v_mfma_i32_16x16x64_i8 v[38:41], v[130:133], v[214:217], v[38:41]
	v_mfma_i32_16x16x64_i8 v[34:37], v[140:143], v[214:217], v[34:37]
	s_waitcnt lgkmcnt(1)
	v_mfma_i32_16x16x64_i8 v[22:25], v[130:133], v[222:225], v[22:25]
	v_mfma_i32_16x16x64_i8 v[18:21], v[140:143], v[222:225], v[18:21]
	v_mfma_i32_16x16x64_i8 v[62:65], v[134:137], v[202:205], v[62:65]
	v_mfma_i32_16x16x64_i8 v[58:61], v[144:147], v[202:205], v[58:61]
	v_mfma_i32_16x16x64_i8 v[46:49], v[134:137], v[210:213], v[46:49]
	v_mfma_i32_16x16x64_i8 v[42:45], v[144:147], v[210:213], v[42:45]
	v_mfma_i32_16x16x64_i8 v[38:41], v[134:137], v[218:221], v[38:41]
	v_mfma_i32_16x16x64_i8 v[34:37], v[144:147], v[218:221], v[34:37]
	s_waitcnt lgkmcnt(0)
	v_mfma_i32_16x16x64_i8 v[22:25], v[134:137], v[226:229], v[22:25]
	v_mfma_i32_16x16x64_i8 v[18:21], v[144:147], v[226:229], v[18:21]
	s_setprio 0
	s_setprio 1
	v_mfma_i32_16x16x64_i8 v[54:57], v[148:151], v[198:201], v[54:57]
	v_mfma_i32_16x16x64_i8 v[50:53], v[156:159], v[198:201], v[50:53]
	v_mfma_i32_16x16x64_i8 v[30:33], v[148:151], v[206:209], v[30:33]
	v_mfma_i32_16x16x64_i8 v[26:29], v[156:159], v[206:209], v[26:29]
	v_mfma_i32_16x16x64_i8 v[14:17], v[148:151], v[214:217], v[14:17]
	v_mfma_i32_16x16x64_i8 v[10:13], v[156:159], v[214:217], v[10:13]
	v_mfma_i32_16x16x64_i8 v[6:9], v[148:151], v[222:225], v[6:9]
	v_mfma_i32_16x16x64_i8 v[2:5], v[156:159], v[222:225], v[2:5]
	s_nop 0
	v_mfma_i32_16x16x64_i8 v[54:57], v[152:155], v[202:205], v[54:57]
	v_mfma_i32_16x16x64_i8 v[50:53], v[194:197], v[202:205], v[50:53]
	v_mfma_i32_16x16x64_i8 v[30:33], v[152:155], v[210:213], v[30:33]
	v_mfma_i32_16x16x64_i8 v[26:29], v[194:197], v[210:213], v[26:29]
	v_mfma_i32_16x16x64_i8 v[14:17], v[152:155], v[218:221], v[14:17]
	v_mfma_i32_16x16x64_i8 v[10:13], v[194:197], v[218:221], v[10:13]
	v_mfma_i32_16x16x64_i8 v[6:9], v[152:155], v[226:229], v[6:9]
	v_mfma_i32_16x16x64_i8 v[2:5], v[194:197], v[226:229], v[2:5]
	s_setprio 0
	s_barrier
	s_add_i32 s11, s11, 2
	s_add_u32 s30, s30, 0x100
	s_addc_u32 s31, s31, 0
	s_cmp_lt_u32 s11, 12
	s_cbranch_scc1 .LBB0_802
	v_readfirstlane_b32 s28, v230
	s_and_b64 s[98:99], s[4:5], exec
	s_cbranch_scc0 .Lp8_nonext
	v_lshl_add_u32 v184, v231, 11, v167
	v_lshl_add_u32 v185, v232, 11, v167
	v_lshl_add_u32 v186, v233, 11, v167
	v_lshl_add_u32 v187, v234, 11, v167
.Lp8_nonext:
	ds_read_b128 v[140:143], v179
	ds_read_b128 v[144:147], v179 offset:1024
	ds_read_b128 v[148:151], v179 offset:2048
	ds_read_b128 v[152:155], v179 offset:3072
	ds_read_b128 v[156:159], v180
	ds_read_b128 v[130:133], v180 offset:1024
	ds_read_b128 v[192:195], v180 offset:2048
	ds_read_b128 v[134:137], v180 offset:3072
	s_ashr_i32 s29, s28, 31
	s_lshl_b64 s[30:31], s[28:29], 23
	s_add_u32 s11, s41, s30
	s_addc_u32 s29, s42, s31
	s_ashr_i32 s27, s26, 31
	s_lshl_b64 s[30:31], s[26:27], 19
	s_add_u32 s30, s11, s30
	s_addc_u32 s31, s29, s31
	s_and_b64 s[4:5], s[4:5], exec
	s_cselect_b32 s5, s31, s35
	s_cselect_b32 s4, s30, s34
	ds_read_b128 v[196:199], v181
	ds_read_b128 v[200:203], v181 offset:1024
	ds_read_b128 v[204:207], v181 offset:2048
	ds_read_b128 v[208:211], v181 offset:3072
	ds_read_b128 v[212:215], v181 offset:4096
	ds_read_b128 v[216:219], v181 offset:5120
	ds_read_b128 v[220:223], v181 offset:6144
	ds_read_b128 v[224:227], v181 offset:7168
	s_mov_b32 s11, m0
	s_mov_b32 m0, s62
	s_nop 0
	global_load_lds_dwordx4 v189, s[20:21]
	s_mov_b32 m0, s63
	s_nop 0
	global_load_lds_dwordx4 v190, s[20:21]
	s_mov_b32 m0, s11
	s_waitcnt vmcnt(8)
	s_waitcnt lgkmcnt(0)
	s_barrier
; #define PG8_STAGEB(bufoff, gbase) glds2(voffB, (gbase), voffB, (gbase) + qstep, ldsb + (bufoff))
; #define PG8_STAGEA(bufoff, rowb, v, h, kb) do { if constexpr (GATHER) glds2((v)[h][0], Ab + (kb), (v)[h][1], Ab + (kb), ldsb + (bufoff)); \
;         else glds2(voffA, Ab + (rowb) + (h) * hstep + (kb), voffA, Ab + (rowb) + (h) * hstep + qstep + (kb), ldsb + (bufoff)); } while (0)
; #define PG8_LDA(dst, b, h) do { _Pragma("unroll") for (int m = 0; m < 4; ++m) _Pragma("unroll") for (int k = 0; k < 2; ++k) dst[m][k] = *(const PG8_LAS bf16x8*)(lds + PG8_SA(b, h) + aoff + m * 2048 + k * 1024); } while (0)
; #define PG8_WAIT_V(n) asm volatile("s_waitcnt vmcnt(" #n ")" ::: "memory")
; #define PG8_WAIT_L(n) asm volatile("s_waitcnt lgkmcnt(" #n ")" ::: "memory")
; #define PG8_BAR __builtin_amdgcn_s_barrier()
; #define PG8_SCHED __builtin_amdgcn_sched_barrier(0)
; template <class Epi, bool GATHER, int MODE, bool SPLIT = false>
; __device__ __forceinline__ void gemm_phase(PG8_LAS unsigned char* lds, const Gemm g, const Order& S, const Epi& E) {
;     ...
;             PG8_WAIT_V(8); PG8_WAIT_L(0); PG8_BAR; PG8_MMA(0, 0, At, B0); PG8_MMA(0, 1, At, B1); PG8_BAR; PG8_SCHED;
;             PG8_LDA(At, 0, 1); PG8_STAGEB(PG8_SB(0, 0), nB); PG8_STAGEB(PG8_SB(0, 1), nB + hstep); PG8_STAGEA(PG8_SA(0, 0), nAr, nv, 0, 0);
;             PG8_WAIT_V(8); PG8_WAIT_L(0); PG8_BAR; PG8_MMA(1, 0, At, B0); PG8_MMA(1, 1, At, B1); PG8_BAR; PG8_SCHED;
	s_setprio 1
	s_waitcnt lgkmcnt(7)
	v_mfma_i32_16x16x64_i8 v[126:129], v[140:143], v[196:199], v[126:129]
	v_mfma_i32_16x16x64_i8 v[122:125], v[148:151], v[196:199], v[122:125]
	s_waitcnt lgkmcnt(5)
	v_mfma_i32_16x16x64_i8 v[118:121], v[140:143], v[204:207], v[118:121]
	v_mfma_i32_16x16x64_i8 v[106:109], v[148:151], v[204:207], v[106:109]
	s_waitcnt lgkmcnt(3)
	v_mfma_i32_16x16x64_i8 v[102:105], v[140:143], v[212:215], v[102:105]
	v_mfma_i32_16x16x64_i8 v[90:93], v[148:151], v[212:215], v[90:93]
	s_waitcnt lgkmcnt(1)
	v_mfma_i32_16x16x64_i8 v[86:89], v[140:143], v[220:223], v[86:89]
	v_mfma_i32_16x16x64_i8 v[74:77], v[148:151], v[220:223], v[74:77]
	v_mfma_i32_16x16x64_i8 v[126:129], v[144:147], v[200:203], v[126:129]
	v_mfma_i32_16x16x64_i8 v[122:125], v[152:155], v[200:203], v[122:125]
	v_mfma_i32_16x16x64_i8 v[118:121], v[144:147], v[208:211], v[118:121]
	v_mfma_i32_16x16x64_i8 v[106:109], v[152:155], v[208:211], v[106:109]
	v_mfma_i32_16x16x64_i8 v[102:105], v[144:147], v[216:219], v[102:105]
	v_mfma_i32_16x16x64_i8 v[90:93], v[152:155], v[216:219], v[90:93]
	s_waitcnt lgkmcnt(0)
	v_mfma_i32_16x16x64_i8 v[86:89], v[144:147], v[224:227], v[86:89]
	v_mfma_i32_16x16x64_i8 v[74:77], v[152:155], v[224:227], v[74:77]
	s_setprio 0
	s_setprio 1
	v_mfma_i32_16x16x64_i8 v[114:117], v[156:159], v[196:199], v[114:117]
	v_mfma_i32_16x16x64_i8 v[110:113], v[192:195], v[196:199], v[110:113]
	v_mfma_i32_16x16x64_i8 v[98:101], v[156:159], v[204:207], v[98:101]
	v_mfma_i32_16x16x64_i8 v[94:97], v[192:195], v[204:207], v[94:97]
	v_mfma_i32_16x16x64_i8 v[82:85], v[156:159], v[212:215], v[82:85]
	v_mfma_i32_16x16x64_i8 v[78:81], v[192:195], v[212:215], v[78:81]
	v_mfma_i32_16x16x64_i8 v[70:73], v[156:159], v[220:223], v[70:73]
	v_mfma_i32_16x16x64_i8 v[66:69], v[192:195], v[220:223], v[66:69]
	s_nop 0
	v_mfma_i32_16x16x64_i8 v[114:117], v[130:133], v[200:203], v[114:117]
	v_mfma_i32_16x16x64_i8 v[110:113], v[134:137], v[200:203], v[110:113]
	v_mfma_i32_16x16x64_i8 v[98:101], v[130:133], v[208:211], v[98:101]
	v_mfma_i32_16x16x64_i8 v[94:97], v[134:137], v[208:211], v[94:97]
	v_mfma_i32_16x16x64_i8 v[82:85], v[130:133], v[216:219], v[82:85]
	v_mfma_i32_16x16x64_i8 v[78:81], v[134:137], v[216:219], v[78:81]
	v_mfma_i32_16x16x64_i8 v[70:73], v[130:133], v[224:227], v[70:73]
	v_mfma_i32_16x16x64_i8 v[66:69], v[134:137], v[224:227], v[66:69]
	s_setprio 0
	s_barrier
	s_add_u32 s34, s4, 0x20000
	ds_read_b128 v[196:199], v181 offset:16384
	ds_read_b128 v[200:203], v181 offset:17408
	ds_read_b128 v[204:207], v181 offset:18432
	ds_read_b128 v[208:211], v181 offset:19456
	ds_read_b128 v[212:215], v181 offset:20480
	ds_read_b128 v[216:219], v181 offset:21504
	ds_read_b128 v[220:223], v181 offset:22528
	ds_read_b128 v[224:227], v181 offset:23552
	s_addc_u32 s35, s5, 0
	s_mov_b32 s11, m0
	s_mov_b32 m0, s49
	s_nop 0
	global_load_lds_dwordx4 v168, s[4:5]
	s_mov_b32 m0, s50
	s_nop 0
	global_load_lds_dwordx4 v168, s[34:35]
	s_mov_b32 m0, s11
	s_add_u32 s34, s4, 0x40000
	s_addc_u32 s35, s5, 0
	s_add_u32 s36, s4, 0x60000
	s_addc_u32 s37, s5, 0
	s_mov_b32 s11, m0
	s_mov_b32 m0, s51
	s_nop 0
	global_load_lds_dwordx4 v168, s[34:35]
	s_mov_b32 m0, s52
	s_nop 0
	global_load_lds_dwordx4 v168, s[36:37]
	s_mov_b32 m0, s11
	s_nop 0
	s_mov_b32 s11, m0
	s_mov_b32 m0, s43
	s_nop 0
	global_load_lds_dwordx4 v184, s[6:7]
	s_mov_b32 m0, s53
	s_nop 0
	global_load_lds_dwordx4 v185, s[6:7]
	s_mov_b32 m0, s11
	s_waitcnt vmcnt(8)
	s_waitcnt lgkmcnt(0)
	s_barrier
	s_setprio 1
	s_waitcnt lgkmcnt(7)
	v_mfma_i32_16x16x64_i8 v[62:65], v[140:143], v[196:199], v[62:65]
	v_mfma_i32_16x16x64_i8 v[58:61], v[148:151], v[196:199], v[58:61]
	s_waitcnt lgkmcnt(5)
	v_mfma_i32_16x16x64_i8 v[46:49], v[140:143], v[204:207], v[46:49]
	v_mfma_i32_16x16x64_i8 v[42:45], v[148:151], v[204:207], v[42:45]
	s_waitcnt lgkmcnt(3)
	v_mfma_i32_16x16x64_i8 v[38:41], v[140:143], v[212:215], v[38:41]
	v_mfma_i32_16x16x64_i8 v[34:37], v[148:151], v[212:215], v[34:37]
	s_waitcnt lgkmcnt(1)
	v_mfma_i32_16x16x64_i8 v[22:25], v[140:143], v[220:223], v[22:25]
	v_mfma_i32_16x16x64_i8 v[18:21], v[148:151], v[220:223], v[18:21]
	v_mfma_i32_16x16x64_i8 v[62:65], v[144:147], v[200:203], v[62:65]
	v_mfma_i32_16x16x64_i8 v[58:61], v[152:155], v[200:203], v[58:61]
	v_mfma_i32_16x16x64_i8 v[46:49], v[144:147], v[208:211], v[46:49]
	v_mfma_i32_16x16x64_i8 v[42:45], v[152:155], v[208:211], v[42:45]
	v_mfma_i32_16x16x64_i8 v[38:41], v[144:147], v[216:219], v[38:41]
	v_mfma_i32_16x16x64_i8 v[34:37], v[152:155], v[216:219], v[34:37]
	s_waitcnt lgkmcnt(0)
	v_mfma_i32_16x16x64_i8 v[22:25], v[144:147], v[224:227], v[22:25]
	v_mfma_i32_16x16x64_i8 v[18:21], v[152:155], v[224:227], v[18:21]
	s_setprio 0
	s_setprio 1
	v_mfma_i32_16x16x64_i8 v[54:57], v[156:159], v[196:199], v[54:57]
	v_mfma_i32_16x16x64_i8 v[50:53], v[192:195], v[196:199], v[50:53]
	v_mfma_i32_16x16x64_i8 v[30:33], v[156:159], v[204:207], v[30:33]
	v_mfma_i32_16x16x64_i8 v[26:29], v[192:195], v[204:207], v[26:29]
	v_mfma_i32_16x16x64_i8 v[14:17], v[156:159], v[212:215], v[14:17]
	v_mfma_i32_16x16x64_i8 v[10:13], v[192:195], v[212:215], v[10:13]
	v_mfma_i32_16x16x64_i8 v[6:9], v[156:159], v[220:223], v[6:9]
	v_mfma_i32_16x16x64_i8 v[2:5], v[192:195], v[220:223], v[2:5]
	s_nop 0
	v_mfma_i32_16x16x64_i8 v[54:57], v[130:133], v[200:203], v[54:57]
	v_mfma_i32_16x16x64_i8 v[50:53], v[134:137], v[200:203], v[50:53]
	v_mfma_i32_16x16x64_i8 v[30:33], v[130:133], v[208:211], v[30:33]
	v_mfma_i32_16x16x64_i8 v[26:29], v[134:137], v[208:211], v[26:29]
	v_mfma_i32_16x16x64_i8 v[14:17], v[130:133], v[216:219], v[14:17]
	v_mfma_i32_16x16x64_i8 v[10:13], v[134:137], v[216:219], v[10:13]
	v_mfma_i32_16x16x64_i8 v[6:9], v[130:133], v[224:227], v[6:9]
	v_mfma_i32_16x16x64_i8 v[2:5], v[134:137], v[224:227], v[2:5]
	s_setprio 0
	s_barrier
; #define PG8_STAGEB(bufoff, gbase) glds2(voffB, (gbase), voffB, (gbase) + qstep, ldsb + (bufoff))
; #define PG8_STAGEA(bufoff, rowb, v, h, kb) do { if constexpr (GATHER) glds2((v)[h][0], Ab + (kb), (v)[h][1], Ab + (kb), ldsb + (bufoff)); \
;         else glds2(voffA, Ab + (rowb) + (h) * hstep + (kb), voffA, Ab + (rowb) + (h) * hstep + qstep + (kb), ldsb + (bufoff)); } while (0)
; #define PG8_LDA(dst, b, h) do { _Pragma("unroll") for (int m = 0; m < 4; ++m) _Pragma("unroll") for (int k = 0; k < 2; ++k) dst[m][k] = *(const PG8_LAS bf16x8*)(lds + PG8_SA(b, h) + aoff + m * 2048 + k * 1024); } while (0)
; #define PG8_LDB(dst, b, h) do { _Pragma("unroll") for (int n = 0; n < 2; ++n) _Pragma("unroll") for (int k = 0; k < 2; ++k) dst[n][k] = *(const PG8_LAS bf16x8*)(lds + PG8_SB(b, h) + boff + n * 2048 + k * 1024); } while (0)
; #define PG8_WAIT_V(n) asm volatile("s_waitcnt vmcnt(" #n ")" ::: "memory")
; #define PG8_WAIT_L(n) asm volatile("s_waitcnt lgkmcnt(" #n ")" ::: "memory")
; #define PG8_BAR __builtin_amdgcn_s_barrier()
; #define PG8_SCHED __builtin_amdgcn_sched_barrier(0)
; template <class Epi, bool GATHER, int MODE, bool SPLIT = false>
; __device__ __forceinline__ void gemm_phase(PG8_LAS unsigned char* lds, const Gemm g, const Order& S, const Epi& E) {
;     ...
;             PG8_LDB(B0, 1, 0); PG8_LDB(B1, 1, 1); PG8_SCHED; PG8_LDA(At, 1, 0); PG8_STAGEA(PG8_SA(0, 1), nAr, nv, 1, 0);
;             PG8_WAIT_V(8); PG8_WAIT_L(0); PG8_BAR; PG8_MMA(0, 0, At, B0); PG8_MMA(0, 1, At, B1); PG8_BAR; PG8_SCHED;
;             PG8_LDA(At, 1, 1); PG8_STAGEB(PG8_SB(1, 0), nB + kstep); PG8_STAGEB(PG8_SB(1, 1), nB + hstep + kstep); PG8_STAGEA(PG8_SA(1, 0), nAr, nv, 0, kstep);
;             PG8_WAIT_V(8); PG8_WAIT_L(0); PG8_BAR; PG8_MMA(1, 0, At, B0); PG8_MMA(1, 1, At, B1); PG8_BAR; PG8_SCHED;
;         }
;         if (wr == 0) PG8_BAR;
	ds_read_b128 v[130:133], v182
	ds_read_b128 v[134:137], v182 offset:1024
	ds_read_b128 v[140:143], v182 offset:2048
	ds_read_b128 v[144:147], v182 offset:3072
	ds_read_b128 v[148:151], v138
	ds_read_b128 v[152:155], v138 offset:1024
	ds_read_b128 v[156:159], v138 offset:2048
	ds_read_b128 v[190:193], v138 offset:3072
	ds_read_b128 v[194:197], v181 offset:32768
	ds_read_b128 v[198:201], v181 offset:33792
	ds_read_b128 v[202:205], v181 offset:34816
	ds_read_b128 v[206:209], v181 offset:35840
	ds_read_b128 v[210:213], v181 offset:36864
	ds_read_b128 v[214:217], v181 offset:37888
	ds_read_b128 v[218:221], v181 offset:38912
	ds_read_b128 v[222:225], v181 offset:39936
	s_mov_b32 s11, m0
	s_mov_b32 m0, s54
	s_nop 0
	global_load_lds_dwordx4 v186, s[6:7]
	s_mov_b32 m0, s55
	s_nop 0
	global_load_lds_dwordx4 v187, s[6:7]
	s_mov_b32 m0, s11
	s_waitcnt vmcnt(8)
	s_waitcnt lgkmcnt(0)
	s_barrier
	s_setprio 1
	s_waitcnt lgkmcnt(7)
	v_mfma_i32_16x16x64_i8 v[126:129], v[130:133], v[194:197], v[126:129]
	v_mfma_i32_16x16x64_i8 v[122:125], v[140:143], v[194:197], v[122:125]
	s_waitcnt lgkmcnt(5)
	v_mfma_i32_16x16x64_i8 v[118:121], v[130:133], v[202:205], v[118:121]
	v_mfma_i32_16x16x64_i8 v[106:109], v[140:143], v[202:205], v[106:109]
	s_waitcnt lgkmcnt(3)
	v_mfma_i32_16x16x64_i8 v[102:105], v[130:133], v[210:213], v[102:105]
	v_mfma_i32_16x16x64_i8 v[90:93], v[140:143], v[210:213], v[90:93]
	s_waitcnt lgkmcnt(1)
	v_mfma_i32_16x16x64_i8 v[86:89], v[130:133], v[218:221], v[86:89]
	v_mfma_i32_16x16x64_i8 v[74:77], v[140:143], v[218:221], v[74:77]
	v_mfma_i32_16x16x64_i8 v[126:129], v[134:137], v[198:201], v[126:129]
	v_mfma_i32_16x16x64_i8 v[122:125], v[144:147], v[198:201], v[122:125]
	v_mfma_i32_16x16x64_i8 v[118:121], v[134:137], v[206:209], v[118:121]
	v_mfma_i32_16x16x64_i8 v[106:109], v[144:147], v[206:209], v[106:109]
	v_mfma_i32_16x16x64_i8 v[102:105], v[134:137], v[214:217], v[102:105]
	v_mfma_i32_16x16x64_i8 v[90:93], v[144:147], v[214:217], v[90:93]
	s_waitcnt lgkmcnt(0)
	v_mfma_i32_16x16x64_i8 v[86:89], v[134:137], v[222:225], v[86:89]
	v_mfma_i32_16x16x64_i8 v[74:77], v[144:147], v[222:225], v[74:77]
	s_setprio 0
	s_setprio 1
	v_mfma_i32_16x16x64_i8 v[114:117], v[148:151], v[194:197], v[114:117]
	v_mfma_i32_16x16x64_i8 v[110:113], v[156:159], v[194:197], v[110:113]
	v_mfma_i32_16x16x64_i8 v[98:101], v[148:151], v[202:205], v[98:101]
	v_mfma_i32_16x16x64_i8 v[94:97], v[156:159], v[202:205], v[94:97]
	v_mfma_i32_16x16x64_i8 v[82:85], v[148:151], v[210:213], v[82:85]
	v_mfma_i32_16x16x64_i8 v[78:81], v[156:159], v[210:213], v[78:81]
	v_mfma_i32_16x16x64_i8 v[70:73], v[148:151], v[218:221], v[70:73]
	v_mfma_i32_16x16x64_i8 v[66:69], v[156:159], v[218:221], v[66:69]
	s_nop 0
	v_mfma_i32_16x16x64_i8 v[114:117], v[152:155], v[198:201], v[114:117]
	v_mfma_i32_16x16x64_i8 v[110:113], v[190:193], v[198:201], v[110:113]
	v_mfma_i32_16x16x64_i8 v[98:101], v[152:155], v[206:209], v[98:101]
	v_mfma_i32_16x16x64_i8 v[94:97], v[190:193], v[206:209], v[94:97]
	v_mfma_i32_16x16x64_i8 v[82:85], v[152:155], v[214:217], v[82:85]
	v_mfma_i32_16x16x64_i8 v[78:81], v[190:193], v[214:217], v[78:81]
	v_mfma_i32_16x16x64_i8 v[70:73], v[152:155], v[222:225], v[70:73]
	v_mfma_i32_16x16x64_i8 v[66:69], v[190:193], v[222:225], v[66:69]
	s_setprio 0
	s_barrier
	s_add_u32 s34, s4, 0x80
	s_addc_u32 s35, s5, 0
	s_add_u32 s36, s4, 0x20080
	ds_read_b128 v[194:197], v181 offset:49152
	ds_read_b128 v[198:201], v181 offset:50176
	ds_read_b128 v[202:205], v181 offset:51200
	ds_read_b128 v[206:209], v181 offset:52224
	ds_read_b128 v[210:213], v181 offset:53248
	ds_read_b128 v[214:217], v181 offset:54272
	ds_read_b128 v[218:221], v181 offset:55296
	ds_read_b128 v[222:225], v181 offset:56320
	s_addc_u32 s37, s5, 0
	s_mov_b32 s11, m0
	s_mov_b32 m0, s56
	s_nop 0
	global_load_lds_dwordx4 v168, s[34:35]
	s_mov_b32 m0, s57
	s_nop 0
	global_load_lds_dwordx4 v168, s[36:37]
	s_mov_b32 m0, s11
	s_add_u32 s34, s4, 0x40080
	s_addc_u32 s35, s5, 0
	s_add_u32 s4, s4, 0x60080
	s_addc_u32 s5, s5, 0
	s_mov_b32 s11, m0
	s_mov_b32 m0, s60
	s_nop 0
	global_load_lds_dwordx4 v168, s[34:35]
	s_mov_b32 m0, s61
	s_nop 0
	global_load_lds_dwordx4 v168, s[4:5]
	s_mov_b32 m0, s11
	s_mov_b32 s4, m0
	s_mov_b32 m0, s58
	s_nop 0
	global_load_lds_dwordx4 v184, s[18:19]
	s_mov_b32 m0, s59
	s_nop 0
	global_load_lds_dwordx4 v185, s[18:19]
	s_mov_b32 m0, s4
	s_waitcnt vmcnt(8)
	s_waitcnt lgkmcnt(0)
	s_barrier
	s_setprio 1
	s_waitcnt lgkmcnt(7)
	v_mfma_i32_16x16x64_i8 v[62:65], v[130:133], v[194:197], v[62:65]
	v_mfma_i32_16x16x64_i8 v[58:61], v[140:143], v[194:197], v[58:61]
	s_waitcnt lgkmcnt(5)
	v_mfma_i32_16x16x64_i8 v[46:49], v[130:133], v[202:205], v[46:49]
	v_mfma_i32_16x16x64_i8 v[42:45], v[140:143], v[202:205], v[42:45]
	s_waitcnt lgkmcnt(3)
	v_mfma_i32_16x16x64_i8 v[38:41], v[130:133], v[210:213], v[38:41]
	v_mfma_i32_16x16x64_i8 v[34:37], v[140:143], v[210:213], v[34:37]
	s_waitcnt lgkmcnt(1)
	v_mfma_i32_16x16x64_i8 v[22:25], v[130:133], v[218:221], v[22:25]
	v_mfma_i32_16x16x64_i8 v[18:21], v[140:143], v[218:221], v[18:21]
	v_mfma_i32_16x16x64_i8 v[62:65], v[134:137], v[198:201], v[62:65]
	v_mfma_i32_16x16x64_i8 v[58:61], v[144:147], v[198:201], v[58:61]
	v_mfma_i32_16x16x64_i8 v[46:49], v[134:137], v[206:209], v[46:49]
	v_mfma_i32_16x16x64_i8 v[42:45], v[144:147], v[206:209], v[42:45]
	v_mfma_i32_16x16x64_i8 v[38:41], v[134:137], v[214:217], v[38:41]
	v_mfma_i32_16x16x64_i8 v[34:37], v[144:147], v[214:217], v[34:37]
	s_waitcnt lgkmcnt(0)
	v_mfma_i32_16x16x64_i8 v[22:25], v[134:137], v[222:225], v[22:25]
	v_mfma_i32_16x16x64_i8 v[18:21], v[144:147], v[222:225], v[18:21]
	s_setprio 0
	s_setprio 1
	v_mfma_i32_16x16x64_i8 v[54:57], v[148:151], v[194:197], v[54:57]
	v_mfma_i32_16x16x64_i8 v[50:53], v[156:159], v[194:197], v[50:53]
	v_mfma_i32_16x16x64_i8 v[30:33], v[148:151], v[202:205], v[30:33]
	v_mfma_i32_16x16x64_i8 v[26:29], v[156:159], v[202:205], v[26:29]
	v_mfma_i32_16x16x64_i8 v[14:17], v[148:151], v[210:213], v[14:17]
	v_mfma_i32_16x16x64_i8 v[10:13], v[156:159], v[210:213], v[10:13]
	v_mfma_i32_16x16x64_i8 v[6:9], v[148:151], v[218:221], v[6:9]
	v_mfma_i32_16x16x64_i8 v[2:5], v[156:159], v[218:221], v[2:5]
	s_nop 0
	v_mfma_i32_16x16x64_i8 v[54:57], v[152:155], v[198:201], v[54:57]
	v_mfma_i32_16x16x64_i8 v[50:53], v[190:193], v[198:201], v[50:53]
	v_mfma_i32_16x16x64_i8 v[30:33], v[152:155], v[206:209], v[30:33]
	v_mfma_i32_16x16x64_i8 v[26:29], v[190:193], v[206:209], v[26:29]
	v_mfma_i32_16x16x64_i8 v[14:17], v[152:155], v[214:217], v[14:17]
	v_mfma_i32_16x16x64_i8 v[10:13], v[190:193], v[214:217], v[10:13]
	v_mfma_i32_16x16x64_i8 v[6:9], v[152:155], v[222:225], v[6:9]
	v_mfma_i32_16x16x64_i8 v[2:5], v[190:193], v[222:225], v[2:5]
	s_setprio 0
	s_barrier
	s_andn2_b64 vcc, exec, s[22:23]
	s_cbranch_vccnz .LBB0_805
	s_barrier

;     __device__ bool next(int i, Unit& u) const {
;         const long L = (long)i * G + c; if (L >= nwg) return false;
;         int wgid = (int)L; { const int q = nwg / NXCD, r = nwg % NXCD, xcd = wgid % NXCD, off = wgid / NXCD; wgid = (xcd < r ? xcd * (q + 1) : r * (q + 1) + (xcd - r) * q) + off; }
;         const int nig = wgm * nN, gid = wgid / nig, fm = gid * wgm, gsz = (nM - fm) < wgm ? (nM - fm) : wgm;
;         u.pm = fm + ((wgid % nig) % gsz); u.pn = (wgid % nig) / gsz; if (u.pn >= gap_at) u.pn += gap; u.e = tile_e ? tile_e[u.pm] : 0; return true;
.LBB0_872:
	s_andn2_b64 vcc, exec, s[28:29]
	s_cbranch_vccnz .LBB0_874
	s_ashr_i32 s1, s26, 31
	s_lshr_b32 s1, s1, 29
	s_add_i32 s1, s26, s1
	s_ashr_i32 s14, s1, 3
	s_and_b32 s1, s1, -8
	s_sub_i32 s1, s26, s1
	s_cmp_lt_i32 s1, 0
	s_cselect_b32 s15, s39, s11
	s_mul_i32 s1, s15, s1
	s_add_i32 s1, s1, s14
	s_ashr_i32 s14, s1, 31
	s_lshr_b32 s14, s14, 27
	s_add_i32 s14, s1, s14
	s_ashr_i32 s15, s14, 5
	s_lshl_b32 s15, s15, 2
	s_sub_i32 s16, s11, s15
	s_min_i32 s16, s16, 4
	s_abs_i32 s17, s16
	v_cvt_f32_u32_e32 v2, s17
	s_sub_i32 s19, 0, s17
	s_andn2_b32 s14, s14, 31
	s_sub_i32 s1, s1, s14
	v_rcp_iflag_f32_e32 v2, v2
	s_abs_i32 s14, s1
	s_xor_b32 s18, s1, s16
	s_ashr_i32 s18, s18, 31
	v_mul_f32_e32 v2, 0x4f7ffffe, v2
	v_cvt_u32_f32_e32 v2, v2
	s_nop 0
	v_readfirstlane_b32 s26, v2
	s_mul_i32 s19, s19, s26
	s_mul_hi_u32 s19, s26, s19
	s_add_i32 s26, s26, s19
	s_mul_hi_u32 s19, s14, s26
	s_mul_i32 s26, s19, s17
	s_sub_i32 s14, s14, s26
	s_add_i32 s27, s19, 1
	s_sub_i32 s26, s14, s17
	s_cmp_ge_u32 s14, s17
	s_cselect_b32 s19, s27, s19
	s_cselect_b32 s14, s26, s14
	s_add_i32 s26, s19, 1
	s_cmp_ge_u32 s14, s17
	s_cselect_b32 s14, s26, s19
	s_xor_b32 s14, s14, s18
	s_sub_i32 s14, s14, s18
	s_mul_i32 s16, s14, s16
	s_sub_i32 s1, s1, s16
	s_add_i32 s16, s1, s15
	s_ashr_i32 s17, s16, 31
	s_lshl_b64 s[18:19], s[16:17], 2
	s_add_u32 s18, s13, s18
	s_addc_u32 s19, s30, s19
	global_load_dword v230, v1, s[18:19]

; #define PG8_STAGEB(bufoff, gbase) glds2(voffB, (gbase), voffB, (gbase) + qstep, ldsb + (bufoff))
; #define PG8_STAGEA(bufoff, rowb, v, h, kb) do { if constexpr (GATHER) glds2((v)[h][0], Ab + (kb), (v)[h][1], Ab + (kb), ldsb + (bufoff)); \
;         else glds2(voffA, Ab + (rowb) + (h) * hstep + (kb), voffA, Ab + (rowb) + (h) * hstep + qstep + (kb), ldsb + (bufoff)); } while (0)
; #define PG8_LDA(dst, b, h) do { _Pragma("unroll") for (int m = 0; m < 4; ++m) _Pragma("unroll") for (int k = 0; k < 2; ++k) dst[m][k] = *(const PG8_LAS bf16x8*)(lds + PG8_SA(b, h) + aoff + m * 2048 + k * 1024); } while (0)
; #define PG8_LDB(dst, b, h) do { _Pragma("unroll") for (int n = 0; n < 2; ++n) _Pragma("unroll") for (int k = 0; k < 2; ++k) dst[n][k] = *(const PG8_LAS bf16x8*)(lds + PG8_SB(b, h) + boff + n * 2048 + k * 1024); } while (0)
; #define PG8_WAIT_V(n) asm volatile("s_waitcnt vmcnt(" #n ")" ::: "memory")
; #define PG8_WAIT_L(n) asm volatile("s_waitcnt lgkmcnt(" #n ")" ::: "memory")
; #define PG8_BAR __builtin_amdgcn_s_barrier()
; template <class Epi, bool GATHER, int MODE, bool SPLIT = false>
; __device__ __forceinline__ void gemm_phase(PG8_LAS unsigned char* lds, const Gemm g, const Order& S, const Epi& E) {
;     ...
;             const size_t k1 = (size_t)(t + 1) * kstep, k2 = k1 + kstep, k3 = k2 + kstep;
;             const char* b2 = cB + k2; const char* b3 = cB + k3;
;             PG8_LDB(B0, 0, 0); PG8_LDB(B1, 0, 1); PG8_SCHED; PG8_LDA(At, 0, 0); PG8_STAGEA(PG8_SA(1, 1), cAr, cv, 1, k1);
;             PG8_WAIT_V(8); PG8_WAIT_L(0); PG8_BAR; PG8_MMA(0, 0, At, B0); PG8_MMA(0, 1, At, B1); PG8_BAR; PG8_SCHED;
;             PG8_LDA(At, 0, 1); PG8_STAGEB(PG8_SB(0, 0), b2); PG8_STAGEB(PG8_SB(0, 1), b2 + hstep); PG8_STAGEA(PG8_SA(0, 0), cAr, cv, 0, k2);
;             PG8_WAIT_V(8); PG8_WAIT_L(0); PG8_BAR; PG8_MMA(1, 0, At, B0); PG8_MMA(1, 1, At, B1); PG8_BAR; PG8_SCHED;
;             PG8_LDB(B0, 1, 0); PG8_LDB(B1, 1, 1); PG8_SCHED; PG8_LDA(At, 1, 0); PG8_STAGEA(PG8_SA(0, 1), cAr, cv, 1, k2);
;             PG8_WAIT_V(8); PG8_WAIT_L(0); PG8_BAR; PG8_MMA(0, 0, At, B0); PG8_MMA(0, 1, At, B1); PG8_BAR; PG8_SCHED;
;             PG8_LDA(At, 1, 1); PG8_STAGEB(PG8_SB(1, 0), b3); PG8_STAGEB(PG8_SB(1, 1), b3 + hstep); PG8_STAGEA(PG8_SA(1, 0), cAr, cv, 0, k3);
;             PG8_WAIT_V(8); PG8_WAIT_L(0); PG8_BAR; PG8_MMA(1, 0, At, B0); PG8_MMA(1, 1, At, B1); PG8_BAR; PG8_SCHED;
.LBB0_875:
	ds_read_b128 v[26:29], v172
	ds_read_b128 v[30:33], v172 offset:1024
	ds_read_b128 v[18:21], v172 offset:2048
	ds_read_b128 v[22:25], v172 offset:3072
	ds_read_b128 v[10:13], v173
	ds_read_b128 v[14:17], v173 offset:1024
	ds_read_b128 v[2:5], v173 offset:2048
	ds_read_b128 v[6:9], v173 offset:3072
	s_add_u32 s63, s24, s26
	s_addc_u32 s64, s25, s27
	s_add_u32 s28, s63, 0x100
	s_addc_u32 s29, s64, 0
	s_add_u32 s65, s15, s26
	ds_read_b128 v[180:183], v174
	ds_read_b128 v[184:187], v174 offset:1024
	ds_read_b128 v[188:191], v174 offset:2048
	ds_read_b128 v[192:195], v174 offset:3072
	ds_read_b128 v[196:199], v174 offset:4096
	ds_read_b128 v[200:203], v174 offset:5120
	ds_read_b128 v[204:207], v174 offset:6144
	ds_read_b128 v[208:211], v174 offset:7168
	s_addc_u32 s66, s19, s27
	s_add_u32 s70, s65, 0x80
	s_addc_u32 s71, s66, 0
	s_add_u32 s67, s58, s26
	s_addc_u32 s68, s59, s27
	s_add_u32 s80, s67, 0x80
	s_addc_u32 s81, s68, 0
	s_mov_b32 s69, m0
	s_mov_b32 m0, s53
	s_nop 0
	global_load_lds_dwordx4 v167, s[70:71]
	s_mov_b32 m0, s54
	s_nop 0
	global_load_lds_dwordx4 v167, s[80:81]
	s_mov_b32 m0, s69
	s_waitcnt vmcnt(8)
	s_waitcnt lgkmcnt(0)
	s_barrier
	s_setprio 1
	s_waitcnt lgkmcnt(6)
	v_mfma_f32_16x16x128_f8f6f4 v[158:161], v[26:33], v[180:187], v[158:161]
	v_mfma_f32_16x16x128_f8f6f4 v[154:157], v[18:25], v[180:187], v[154:157]
	s_waitcnt lgkmcnt(4)
	v_mfma_f32_16x16x128_f8f6f4 v[150:153], v[26:33], v[188:195], v[150:153]
	v_mfma_f32_16x16x128_f8f6f4 v[146:149], v[18:25], v[188:195], v[146:149]
	s_waitcnt lgkmcnt(2)
	v_mfma_f32_16x16x128_f8f6f4 v[142:145], v[26:33], v[196:203], v[142:145]
	v_mfma_f32_16x16x128_f8f6f4 v[138:141], v[18:25], v[196:203], v[138:141]
	s_waitcnt lgkmcnt(0)
	v_mfma_f32_16x16x128_f8f6f4 v[134:137], v[26:33], v[204:211], v[134:137]
	v_mfma_f32_16x16x128_f8f6f4 v[130:133], v[18:25], v[204:211], v[130:133]
	s_setprio 0
	s_setprio 1
	v_mfma_f32_16x16x128_f8f6f4 v[126:129], v[10:17], v[180:187], v[126:129]
	v_mfma_f32_16x16x128_f8f6f4 v[122:125], v[2:9], v[180:187], v[122:125]
	v_mfma_f32_16x16x128_f8f6f4 v[118:121], v[10:17], v[188:195], v[118:121]
	v_mfma_f32_16x16x128_f8f6f4 v[114:117], v[2:9], v[188:195], v[114:117]
	v_mfma_f32_16x16x128_f8f6f4 v[110:113], v[10:17], v[196:203], v[110:113]
	v_mfma_f32_16x16x128_f8f6f4 v[106:109], v[2:9], v[196:203], v[106:109]
	v_mfma_f32_16x16x128_f8f6f4 v[102:105], v[10:17], v[204:211], v[102:105]
	v_mfma_f32_16x16x128_f8f6f4 v[98:101], v[2:9], v[204:211], v[98:101]
	s_setprio 0
	s_barrier
	s_add_u32 s70, s63, 0x20100
	s_addc_u32 s71, s64, 0
	ds_read_b128 v[180:183], v174 offset:16384
	ds_read_b128 v[184:187], v174 offset:17408
	ds_read_b128 v[188:191], v174 offset:18432
	ds_read_b128 v[192:195], v174 offset:19456
	ds_read_b128 v[196:199], v174 offset:20480
	ds_read_b128 v[200:203], v174 offset:21504
	ds_read_b128 v[204:207], v174 offset:22528
	ds_read_b128 v[208:211], v174 offset:23552
	s_mov_b32 s69, m0
	s_mov_b32 m0, s21
	s_nop 0
	global_load_lds_dwordx4 v166, s[28:29]
	s_mov_b32 m0, s41
	s_nop 0
	global_load_lds_dwordx4 v166, s[70:71]
	s_mov_b32 m0, s69
	s_add_u32 s28, s63, 0x40100
	s_addc_u32 s29, s64, 0
	s_add_u32 s70, s63, 0x60100
	s_addc_u32 s71, s64, 0
	s_mov_b32 s69, m0
	s_mov_b32 m0, s42
	s_nop 0
	global_load_lds_dwordx4 v166, s[28:29]
	s_mov_b32 m0, s43
	s_nop 0
	global_load_lds_dwordx4 v166, s[70:71]
	s_mov_b32 m0, s69
	s_add_u32 s28, s1, s26
	s_addc_u32 s29, s57, s27
	s_add_u32 s80, s28, 0x100
	s_addc_u32 s81, s29, 0
	s_add_u32 s69, s60, s26
	s_addc_u32 s70, s61, s27
	s_add_u32 s82, s69, 0x100
	s_addc_u32 s83, s70, 0
	s_mov_b32 s71, m0
	s_mov_b32 m0, s37
	s_nop 0
	global_load_lds_dwordx4 v167, s[80:81]
	s_mov_b32 m0, s44
	s_nop 0
	global_load_lds_dwordx4 v167, s[82:83]
	s_mov_b32 m0, s71
	s_waitcnt vmcnt(8)
	s_waitcnt lgkmcnt(0)
	s_barrier
	s_setprio 1
	s_waitcnt lgkmcnt(6)
	v_mfma_f32_16x16x128_f8f6f4 v[94:97], v[26:33], v[180:187], v[94:97]
	v_mfma_f32_16x16x128_f8f6f4 v[90:93], v[18:25], v[180:187], v[90:93]
	s_waitcnt lgkmcnt(4)
	v_mfma_f32_16x16x128_f8f6f4 v[86:89], v[26:33], v[188:195], v[86:89]
	v_mfma_f32_16x16x128_f8f6f4 v[82:85], v[18:25], v[188:195], v[82:85]
	s_waitcnt lgkmcnt(2)
	v_mfma_f32_16x16x128_f8f6f4 v[78:81], v[26:33], v[196:203], v[78:81]
	v_mfma_f32_16x16x128_f8f6f4 v[74:77], v[18:25], v[196:203], v[74:77]
	s_waitcnt lgkmcnt(0)
	v_mfma_f32_16x16x128_f8f6f4 v[70:73], v[26:33], v[204:211], v[70:73]
	v_mfma_f32_16x16x128_f8f6f4 v[66:69], v[18:25], v[204:211], v[66:69]
	s_setprio 0
	s_setprio 1
	v_mfma_f32_16x16x128_f8f6f4 v[62:65], v[10:17], v[180:187], v[62:65]
	v_mfma_f32_16x16x128_f8f6f4 v[58:61], v[2:9], v[180:187], v[58:61]
	v_mfma_f32_16x16x128_f8f6f4 v[54:57], v[10:17], v[188:195], v[54:57]
	v_mfma_f32_16x16x128_f8f6f4 v[50:53], v[2:9], v[188:195], v[50:53]
	v_mfma_f32_16x16x128_f8f6f4 v[46:49], v[10:17], v[196:203], v[46:49]
	v_mfma_f32_16x16x128_f8f6f4 v[42:45], v[2:9], v[196:203], v[42:45]
	v_mfma_f32_16x16x128_f8f6f4 v[38:41], v[10:17], v[204:211], v[38:41]
	v_mfma_f32_16x16x128_f8f6f4 v[34:37], v[2:9], v[204:211], v[34:37]
	s_setprio 0
	s_barrier
	ds_read_b128 v[18:21], v175
	ds_read_b128 v[22:25], v175 offset:1024
	ds_read_b128 v[26:29], v175 offset:2048
	ds_read_b128 v[30:33], v175 offset:3072
	ds_read_b128 v[10:13], v176
	ds_read_b128 v[14:17], v176 offset:1024
	ds_read_b128 v[2:5], v176 offset:2048
	ds_read_b128 v[6:9], v176 offset:3072
	ds_read_b128 v[180:183], v174 offset:32768
	ds_read_b128 v[184:187], v174 offset:33792
	ds_read_b128 v[188:191], v174 offset:34816
	ds_read_b128 v[192:195], v174 offset:35840
	ds_read_b128 v[196:199], v174 offset:36864
	ds_read_b128 v[200:203], v174 offset:37888
	ds_read_b128 v[204:207], v174 offset:38912
	ds_read_b128 v[208:211], v174 offset:39936
	s_add_u32 s80, s65, 0x100
	s_addc_u32 s81, s66, 0
	s_add_u32 s66, s67, 0x100
	s_addc_u32 s67, s68, 0
	s_mov_b32 s65, m0
	s_mov_b32 m0, s45
	s_nop 0
	global_load_lds_dwordx4 v167, s[80:81]
	s_mov_b32 m0, s46
	s_nop 0
	global_load_lds_dwordx4 v167, s[66:67]
	s_mov_b32 m0, s65
	s_waitcnt vmcnt(8)
	s_waitcnt lgkmcnt(0)
	s_barrier
; #define PG8_STAGEB(bufoff, gbase) glds2(voffB, (gbase), voffB, (gbase) + qstep, ldsb + (bufoff))
; #define PG8_STAGEA(bufoff, rowb, v, h, kb) do { if constexpr (GATHER) glds2((v)[h][0], Ab + (kb), (v)[h][1], Ab + (kb), ldsb + (bufoff)); \
;         else glds2(voffA, Ab + (rowb) + (h) * hstep + (kb), voffA, Ab + (rowb) + (h) * hstep + qstep + (kb), ldsb + (bufoff)); } while (0)
; #define PG8_LDA(dst, b, h) do { _Pragma("unroll") for (int m = 0; m < 4; ++m) _Pragma("unroll") for (int k = 0; k < 2; ++k) dst[m][k] = *(const PG8_LAS bf16x8*)(lds + PG8_SA(b, h) + aoff + m * 2048 + k * 1024); } while (0)
; #define PG8_LDB(dst, b, h) do { _Pragma("unroll") for (int n = 0; n < 2; ++n) _Pragma("unroll") for (int k = 0; k < 2; ++k) dst[n][k] = *(const PG8_LAS bf16x8*)(lds + PG8_SB(b, h) + boff + n * 2048 + k * 1024); } while (0)
; #define PG8_WAIT_V(n) asm volatile("s_waitcnt vmcnt(" #n ")" ::: "memory")
; #define PG8_WAIT_L(n) asm volatile("s_waitcnt lgkmcnt(" #n ")" ::: "memory")
; #define PG8_BAR __builtin_amdgcn_s_barrier()
; #define PG8_SCHED __builtin_amdgcn_sched_barrier(0)
; template <class Epi, bool GATHER, int MODE, bool SPLIT = false>
; __device__ __forceinline__ void gemm_phase(PG8_LAS unsigned char* lds, const Gemm g, const Order& S, const Epi& E) {
;     ...
;         const char* nB = has_next ? (const char*)g.Bt + (size_t)nxt.e * g.bstride + (size_t)nxt.pn * tstep : cB;
;         const size_t nAr = has_next ? (size_t)nxt.pm * tstep : cAr;
;     ...
;             PG8_WAIT_V(8); PG8_WAIT_L(0); PG8_BAR; PG8_MMA(0, 0, At, B0); PG8_MMA(0, 1, At, B1); PG8_BAR; PG8_SCHED;
;             PG8_LDA(At, 1, 1); PG8_STAGEB(PG8_SB(1, 0), b3); PG8_STAGEB(PG8_SB(1, 1), b3 + hstep); PG8_STAGEA(PG8_SA(1, 0), cAr, cv, 0, k3);
;             PG8_WAIT_V(8); PG8_WAIT_L(0); PG8_BAR; PG8_MMA(1, 0, At, B0); PG8_MMA(1, 1, At, B1); PG8_BAR; PG8_SCHED;
;         }
;         {
;             const size_t k1 = (size_t)(nt - 1) * kstep;
;             PG8_LDB(B0, 0, 0); PG8_LDB(B1, 0, 1); PG8_SCHED; PG8_LDA(At, 0, 0); PG8_STAGEA(PG8_SA(1, 1), cAr, cv, 1, k1);
;             PG8_WAIT_V(8); PG8_WAIT_L(0); PG8_BAR; PG8_MMA(0, 0, At, B0); PG8_MMA(0, 1, At, B1); PG8_BAR; PG8_SCHED;
;             PG8_LDA(At, 0, 1); PG8_STAGEB(PG8_SB(0, 0), nB); PG8_STAGEB(PG8_SB(0, 1), nB + hstep); PG8_STAGEA(PG8_SA(0, 0), nAr, nv, 0, 0);
	s_setprio 1
	s_waitcnt lgkmcnt(6)
	v_mfma_f32_16x16x128_f8f6f4 v[158:161], v[18:25], v[180:187], v[158:161]
	v_mfma_f32_16x16x128_f8f6f4 v[154:157], v[26:33], v[180:187], v[154:157]
	s_waitcnt lgkmcnt(4)
	v_mfma_f32_16x16x128_f8f6f4 v[150:153], v[18:25], v[188:195], v[150:153]
	v_mfma_f32_16x16x128_f8f6f4 v[146:149], v[26:33], v[188:195], v[146:149]
	s_waitcnt lgkmcnt(2)
	v_mfma_f32_16x16x128_f8f6f4 v[142:145], v[18:25], v[196:203], v[142:145]
	v_mfma_f32_16x16x128_f8f6f4 v[138:141], v[26:33], v[196:203], v[138:141]
	s_waitcnt lgkmcnt(0)
	v_mfma_f32_16x16x128_f8f6f4 v[134:137], v[18:25], v[204:211], v[134:137]
	v_mfma_f32_16x16x128_f8f6f4 v[130:133], v[26:33], v[204:211], v[130:133]
	s_setprio 0
	s_setprio 1
	v_mfma_f32_16x16x128_f8f6f4 v[126:129], v[10:17], v[180:187], v[126:129]
	v_mfma_f32_16x16x128_f8f6f4 v[122:125], v[2:9], v[180:187], v[122:125]
	v_mfma_f32_16x16x128_f8f6f4 v[118:121], v[10:17], v[188:195], v[118:121]
	v_mfma_f32_16x16x128_f8f6f4 v[114:117], v[2:9], v[188:195], v[114:117]
	v_mfma_f32_16x16x128_f8f6f4 v[110:113], v[10:17], v[196:203], v[110:113]
	v_mfma_f32_16x16x128_f8f6f4 v[106:109], v[2:9], v[196:203], v[106:109]
	v_mfma_f32_16x16x128_f8f6f4 v[102:105], v[10:17], v[204:211], v[102:105]
	v_mfma_f32_16x16x128_f8f6f4 v[98:101], v[2:9], v[204:211], v[98:101]
	s_setprio 0
	s_barrier
	s_add_u32 s66, s63, 0x180
	s_addc_u32 s67, s64, 0
	s_add_u32 s80, s63, 0x20180
	s_addc_u32 s81, s64, 0
	ds_read_b128 v[180:183], v174 offset:49152
	ds_read_b128 v[184:187], v174 offset:50176
	ds_read_b128 v[188:191], v174 offset:51200
	ds_read_b128 v[192:195], v174 offset:52224
	ds_read_b128 v[196:199], v174 offset:53248
	ds_read_b128 v[200:203], v174 offset:54272
	ds_read_b128 v[204:207], v174 offset:55296
	ds_read_b128 v[208:211], v174 offset:56320
	s_mov_b32 s65, m0
	s_mov_b32 m0, s47
	s_nop 0
	global_load_lds_dwordx4 v166, s[66:67]
	s_mov_b32 m0, s48
	s_nop 0
	global_load_lds_dwordx4 v166, s[80:81]
	s_mov_b32 m0, s65
	s_add_u32 s66, s63, 0x40180
	s_addc_u32 s67, s64, 0
	s_add_u32 s80, s63, 0x60180
	s_addc_u32 s81, s64, 0
	s_add_u32 s28, s28, 0x180
	s_addc_u32 s29, s29, 0
	s_mov_b32 s63, m0
	s_mov_b32 m0, s51
	s_nop 0
	global_load_lds_dwordx4 v166, s[66:67]
	s_mov_b32 m0, s52
	s_nop 0
	global_load_lds_dwordx4 v166, s[80:81]
	s_mov_b32 m0, s63
	s_add_u32 s64, s69, 0x180
	s_addc_u32 s65, s70, 0
	s_mov_b32 s63, m0
	s_mov_b32 m0, s49
	s_nop 0
	global_load_lds_dwordx4 v167, s[28:29]
	s_mov_b32 m0, s50
	s_nop 0
	global_load_lds_dwordx4 v167, s[64:65]
	s_mov_b32 m0, s63
	s_waitcnt vmcnt(8)
	s_waitcnt lgkmcnt(0)
	s_barrier
	s_setprio 1
	s_waitcnt lgkmcnt(6)
	v_mfma_f32_16x16x128_f8f6f4 v[94:97], v[18:25], v[180:187], v[94:97]
	v_mfma_f32_16x16x128_f8f6f4 v[90:93], v[26:33], v[180:187], v[90:93]
	s_waitcnt lgkmcnt(4)
	v_mfma_f32_16x16x128_f8f6f4 v[86:89], v[18:25], v[188:195], v[86:89]
	v_mfma_f32_16x16x128_f8f6f4 v[82:85], v[26:33], v[188:195], v[82:85]
	s_waitcnt lgkmcnt(2)
	v_mfma_f32_16x16x128_f8f6f4 v[78:81], v[18:25], v[196:203], v[78:81]
	v_mfma_f32_16x16x128_f8f6f4 v[74:77], v[26:33], v[196:203], v[74:77]
	s_waitcnt lgkmcnt(0)
	v_mfma_f32_16x16x128_f8f6f4 v[70:73], v[18:25], v[204:211], v[70:73]
	v_mfma_f32_16x16x128_f8f6f4 v[66:69], v[26:33], v[204:211], v[66:69]
	s_setprio 0
	s_setprio 1
	v_mfma_f32_16x16x128_f8f6f4 v[62:65], v[10:17], v[180:187], v[62:65]
	v_mfma_f32_16x16x128_f8f6f4 v[58:61], v[2:9], v[180:187], v[58:61]
	v_mfma_f32_16x16x128_f8f6f4 v[54:57], v[10:17], v[188:195], v[54:57]
	v_mfma_f32_16x16x128_f8f6f4 v[50:53], v[2:9], v[188:195], v[50:53]
	v_mfma_f32_16x16x128_f8f6f4 v[46:49], v[10:17], v[196:203], v[46:49]
	v_mfma_f32_16x16x128_f8f6f4 v[42:45], v[2:9], v[196:203], v[42:45]
	v_mfma_f32_16x16x128_f8f6f4 v[38:41], v[10:17], v[204:211], v[38:41]
	v_mfma_f32_16x16x128_f8f6f4 v[34:37], v[2:9], v[204:211], v[34:37]
	s_setprio 0
	s_barrier
	s_add_i32 s62, s62, 2
	s_add_u32 s26, s26, 0x100
	s_addc_u32 s27, s27, 0
	s_cmp_lt_u32 s62, 12
	s_cbranch_scc1 .LBB0_875
	v_readfirstlane_b32 s18, v230
	ds_read_b128 v[26:29], v172
	ds_read_b128 v[30:33], v172 offset:1024
	ds_read_b128 v[18:21], v172 offset:2048
	ds_read_b128 v[22:25], v172 offset:3072
	ds_read_b128 v[10:13], v173
	ds_read_b128 v[14:17], v173 offset:1024
	ds_read_b128 v[2:5], v173 offset:2048
	ds_read_b128 v[6:9], v173 offset:3072
	s_ashr_i32 s19, s18, 31
	s_lshl_b64 s[26:27], s[18:19], 22
	s_add_u32 s19, s35, s26
	s_addc_u32 s28, s36, s27
	s_ashr_i32 s15, s14, 31
	s_lshl_b64 s[26:27], s[14:15], 19
	s_add_u32 s26, s19, s26
	s_addc_u32 s27, s28, s27
	s_lshl_b64 s[28:29], s[16:17], 19
	s_and_b64 s[58:59], exec, s[2:3]
	s_cselect_b32 s25, s27, s25
	s_cselect_b32 s24, s26, s24
	s_cselect_b32 s15, s29, s23
	s_cselect_b32 s17, s28, s22
	ds_read_b128 v[180:183], v174
	ds_read_b128 v[184:187], v174 offset:1024
	ds_read_b128 v[188:191], v174 offset:2048
	ds_read_b128 v[192:195], v174 offset:3072
	ds_read_b128 v[196:199], v174 offset:4096
	ds_read_b128 v[200:203], v174 offset:5120
	ds_read_b128 v[204:207], v174 offset:6144
	ds_read_b128 v[208:211], v174 offset:7168
	s_add_u32 s22, s1, 0x40780
	s_addc_u32 s23, s57, 0
	s_add_u32 s58, s1, 0x60780
	s_addc_u32 s59, s57, 0
	s_mov_b32 s1, m0
	s_mov_b32 m0, s53
	s_nop 0
	global_load_lds_dwordx4 v167, s[22:23]
	s_mov_b32 m0, s54
	s_nop 0
	global_load_lds_dwordx4 v167, s[58:59]
	s_mov_b32 m0, s1
	s_waitcnt vmcnt(8)
	s_waitcnt lgkmcnt(0)
	s_barrier
; #define PG8_STAGEB(bufoff, gbase) glds2(voffB, (gbase), voffB, (gbase) + qstep, ldsb + (bufoff))
; #define PG8_STAGEA(bufoff, rowb, v, h, kb) do { if constexpr (GATHER) glds2((v)[h][0], Ab + (kb), (v)[h][1], Ab + (kb), ldsb + (bufoff)); \
;         else glds2(voffA, Ab + (rowb) + (h) * hstep + (kb), voffA, Ab + (rowb) + (h) * hstep + qstep + (kb), ldsb + (bufoff)); } while (0)
; #define PG8_LDA(dst, b, h) do { _Pragma("unroll") for (int m = 0; m < 4; ++m) _Pragma("unroll") for (int k = 0; k < 2; ++k) dst[m][k] = *(const PG8_LAS bf16x8*)(lds + PG8_SA(b, h) + aoff + m * 2048 + k * 1024); } while (0)
; #define PG8_LDB(dst, b, h) do { _Pragma("unroll") for (int n = 0; n < 2; ++n) _Pragma("unroll") for (int k = 0; k < 2; ++k) dst[n][k] = *(const PG8_LAS bf16x8*)(lds + PG8_SB(b, h) + boff + n * 2048 + k * 1024); } while (0)
; #define PG8_WAIT_V(n) asm volatile("s_waitcnt vmcnt(" #n ")" ::: "memory")
; #define PG8_WAIT_L(n) asm volatile("s_waitcnt lgkmcnt(" #n ")" ::: "memory")
; #define PG8_BAR __builtin_amdgcn_s_barrier()
; #define PG8_SCHED __builtin_amdgcn_sched_barrier(0)
; template <class Epi, bool GATHER, int MODE, bool SPLIT = false>
; __device__ __forceinline__ void gemm_phase(PG8_LAS unsigned char* lds, const Gemm g, const Order& S, const Epi& E) {
;     ...
;             PG8_LDB(B0, 0, 0); PG8_LDB(B1, 0, 1); PG8_SCHED; PG8_LDA(At, 0, 0); PG8_STAGEA(PG8_SA(1, 1), cAr, cv, 1, k1);
;             PG8_WAIT_V(8); PG8_WAIT_L(0); PG8_BAR; PG8_MMA(0, 0, At, B0); PG8_MMA(0, 1, At, B1); PG8_BAR; PG8_SCHED;
;             PG8_LDA(At, 0, 1); PG8_STAGEB(PG8_SB(0, 0), nB); PG8_STAGEB(PG8_SB(0, 1), nB + hstep); PG8_STAGEA(PG8_SA(0, 0), nAr, nv, 0, 0);
;             PG8_WAIT_V(8); PG8_WAIT_L(0); PG8_BAR; PG8_MMA(1, 0, At, B0); PG8_MMA(1, 1, At, B1); PG8_BAR; PG8_SCHED;
;             PG8_LDB(B0, 1, 0); PG8_LDB(B1, 1, 1); PG8_SCHED; PG8_LDA(At, 1, 0); PG8_STAGEA(PG8_SA(0, 1), nAr, nv, 1, 0);
;             PG8_WAIT_V(8); PG8_WAIT_L(0); PG8_BAR; PG8_MMA(0, 0, At, B0); PG8_MMA(0, 1, At, B1); PG8_BAR; PG8_SCHED;
	s_setprio 1
	s_waitcnt lgkmcnt(6)
	v_mfma_f32_16x16x128_f8f6f4 v[158:161], v[26:33], v[180:187], v[158:161]
	v_mfma_f32_16x16x128_f8f6f4 v[154:157], v[18:25], v[180:187], v[154:157]
	s_waitcnt lgkmcnt(4)
	v_mfma_f32_16x16x128_f8f6f4 v[150:153], v[26:33], v[188:195], v[150:153]
	v_mfma_f32_16x16x128_f8f6f4 v[146:149], v[18:25], v[188:195], v[146:149]
	s_waitcnt lgkmcnt(2)
	v_mfma_f32_16x16x128_f8f6f4 v[142:145], v[26:33], v[196:203], v[142:145]
	v_mfma_f32_16x16x128_f8f6f4 v[138:141], v[18:25], v[196:203], v[138:141]
	s_waitcnt lgkmcnt(0)
	v_mfma_f32_16x16x128_f8f6f4 v[134:137], v[26:33], v[204:211], v[134:137]
	v_mfma_f32_16x16x128_f8f6f4 v[130:133], v[18:25], v[204:211], v[130:133]
	s_setprio 0
	s_setprio 1
	v_mfma_f32_16x16x128_f8f6f4 v[126:129], v[10:17], v[180:187], v[126:129]
	v_mfma_f32_16x16x128_f8f6f4 v[122:125], v[2:9], v[180:187], v[122:125]
	v_mfma_f32_16x16x128_f8f6f4 v[118:121], v[10:17], v[188:195], v[118:121]
	v_mfma_f32_16x16x128_f8f6f4 v[114:117], v[2:9], v[188:195], v[114:117]
	v_mfma_f32_16x16x128_f8f6f4 v[110:113], v[10:17], v[196:203], v[110:113]
	v_mfma_f32_16x16x128_f8f6f4 v[106:109], v[2:9], v[196:203], v[106:109]
	v_mfma_f32_16x16x128_f8f6f4 v[102:105], v[10:17], v[204:211], v[102:105]
	v_mfma_f32_16x16x128_f8f6f4 v[98:101], v[2:9], v[204:211], v[98:101]
	s_setprio 0
	s_barrier
	s_add_u32 s22, s24, 0x20000
	s_addc_u32 s23, s25, 0
	ds_read_b128 v[180:183], v174 offset:16384
	ds_read_b128 v[184:187], v174 offset:17408
	ds_read_b128 v[188:191], v174 offset:18432
	ds_read_b128 v[192:195], v174 offset:19456
	ds_read_b128 v[196:199], v174 offset:20480
	ds_read_b128 v[200:203], v174 offset:21504
	ds_read_b128 v[204:207], v174 offset:22528
	ds_read_b128 v[208:211], v174 offset:23552
	s_mov_b32 s1, m0
	s_mov_b32 m0, s21
	s_nop 0
	global_load_lds_dwordx4 v166, s[24:25]
	s_mov_b32 m0, s41
	s_nop 0
	global_load_lds_dwordx4 v166, s[22:23]
	s_mov_b32 m0, s1
	s_add_u32 s22, s24, 0x40000
	s_addc_u32 s23, s25, 0
	s_add_u32 s58, s24, 0x60000
	s_addc_u32 s59, s25, 0
	s_mov_b32 s1, m0
	s_mov_b32 m0, s42
	s_nop 0
	global_load_lds_dwordx4 v166, s[22:23]
	s_mov_b32 m0, s43
	s_nop 0
	global_load_lds_dwordx4 v166, s[58:59]
	s_mov_b32 m0, s1
	s_add_u32 s22, s31, s17
	s_addc_u32 s23, s34, s15
	s_add_u32 s58, s22, 0x20000
	s_addc_u32 s59, s23, 0
	s_mov_b32 s1, m0
	s_mov_b32 m0, s37
	s_nop 0
	global_load_lds_dwordx4 v167, s[22:23]
	s_mov_b32 m0, s44
	s_nop 0
	global_load_lds_dwordx4 v167, s[58:59]
	s_mov_b32 m0, s1
	s_waitcnt vmcnt(8)
	s_waitcnt lgkmcnt(0)
	s_barrier
	s_setprio 1
	s_waitcnt lgkmcnt(6)
	v_mfma_f32_16x16x128_f8f6f4 v[94:97], v[26:33], v[180:187], v[94:97]
	v_mfma_f32_16x16x128_f8f6f4 v[90:93], v[18:25], v[180:187], v[90:93]
	s_waitcnt lgkmcnt(4)
	v_mfma_f32_16x16x128_f8f6f4 v[86:89], v[26:33], v[188:195], v[86:89]
	v_mfma_f32_16x16x128_f8f6f4 v[82:85], v[18:25], v[188:195], v[82:85]
	s_waitcnt lgkmcnt(2)
	v_mfma_f32_16x16x128_f8f6f4 v[78:81], v[26:33], v[196:203], v[78:81]
	v_mfma_f32_16x16x128_f8f6f4 v[74:77], v[18:25], v[196:203], v[74:77]
	s_waitcnt lgkmcnt(0)
	v_mfma_f32_16x16x128_f8f6f4 v[70:73], v[26:33], v[204:211], v[70:73]
	v_mfma_f32_16x16x128_f8f6f4 v[66:69], v[18:25], v[204:211], v[66:69]
	s_setprio 0
	s_setprio 1
	v_mfma_f32_16x16x128_f8f6f4 v[62:65], v[10:17], v[180:187], v[62:65]
	v_mfma_f32_16x16x128_f8f6f4 v[58:61], v[2:9], v[180:187], v[58:61]
	v_mfma_f32_16x16x128_f8f6f4 v[54:57], v[10:17], v[188:195], v[54:57]
	v_mfma_f32_16x16x128_f8f6f4 v[50:53], v[2:9], v[188:195], v[50:53]
	v_mfma_f32_16x16x128_f8f6f4 v[46:49], v[10:17], v[196:203], v[46:49]
	v_mfma_f32_16x16x128_f8f6f4 v[42:45], v[2:9], v[196:203], v[42:45]
	v_mfma_f32_16x16x128_f8f6f4 v[38:41], v[10:17], v[204:211], v[38:41]
	v_mfma_f32_16x16x128_f8f6f4 v[34:37], v[2:9], v[204:211], v[34:37]
	s_setprio 0
	s_barrier
	ds_read_b128 v[26:29], v175
	ds_read_b128 v[30:33], v175 offset:1024
	ds_read_b128 v[18:21], v175 offset:2048
	ds_read_b128 v[22:25], v175 offset:3072
	ds_read_b128 v[10:13], v176
	ds_read_b128 v[14:17], v176 offset:1024
	ds_read_b128 v[2:5], v176 offset:2048
	ds_read_b128 v[6:9], v176 offset:3072
	ds_read_b128 v[180:183], v174 offset:32768
	ds_read_b128 v[184:187], v174 offset:33792
	ds_read_b128 v[188:191], v174 offset:34816
	ds_read_b128 v[192:195], v174 offset:35840
	ds_read_b128 v[196:199], v174 offset:36864
	ds_read_b128 v[200:203], v174 offset:37888
	ds_read_b128 v[204:207], v174 offset:38912
	ds_read_b128 v[208:211], v174 offset:39936
	s_add_u32 s58, s22, 0x40000
	s_addc_u32 s59, s23, 0
	s_add_u32 s60, s22, 0x60000
	s_addc_u32 s61, s23, 0
	s_mov_b32 s1, m0
	s_mov_b32 m0, s45
	s_nop 0
	global_load_lds_dwordx4 v167, s[58:59]
	s_mov_b32 m0, s46
	s_nop 0
	global_load_lds_dwordx4 v167, s[60:61]
	s_mov_b32 m0, s1
	s_waitcnt vmcnt(8)
	s_waitcnt lgkmcnt(0)
	s_barrier
; #define PG8_STAGEB(bufoff, gbase) glds2(voffB, (gbase), voffB, (gbase) + qstep, ldsb + (bufoff))
; #define PG8_STAGEA(bufoff, rowb, v, h, kb) do { if constexpr (GATHER) glds2((v)[h][0], Ab + (kb), (v)[h][1], Ab + (kb), ldsb + (bufoff)); \
;         else glds2(voffA, Ab + (rowb) + (h) * hstep + (kb), voffA, Ab + (rowb) + (h) * hstep + qstep + (kb), ldsb + (bufoff)); } while (0)
; #define PG8_LDA(dst, b, h) do { _Pragma("unroll") for (int m = 0; m < 4; ++m) _Pragma("unroll") for (int k = 0; k < 2; ++k) dst[m][k] = *(const PG8_LAS bf16x8*)(lds + PG8_SA(b, h) + aoff + m * 2048 + k * 1024); } while (0)
; #define PG8_WAIT_V(n) asm volatile("s_waitcnt vmcnt(" #n ")" ::: "memory")
; #define PG8_WAIT_L(n) asm volatile("s_waitcnt lgkmcnt(" #n ")" ::: "memory")
; #define PG8_BAR __builtin_amdgcn_s_barrier()
; #define PG8_SCHED __builtin_amdgcn_sched_barrier(0)
; template <class Epi, bool GATHER, int MODE, bool SPLIT = false>
; __device__ __forceinline__ void gemm_phase(PG8_LAS unsigned char* lds, const Gemm g, const Order& S, const Epi& E) {
;     ...
;             PG8_WAIT_V(8); PG8_WAIT_L(0); PG8_BAR; PG8_MMA(0, 0, At, B0); PG8_MMA(0, 1, At, B1); PG8_BAR; PG8_SCHED;
;             PG8_LDA(At, 1, 1); PG8_STAGEB(PG8_SB(1, 0), nB + kstep); PG8_STAGEB(PG8_SB(1, 1), nB + hstep + kstep); PG8_STAGEA(PG8_SA(1, 0), nAr, nv, 0, kstep);
;             PG8_WAIT_V(8); PG8_WAIT_L(0); PG8_BAR; PG8_MMA(1, 0, At, B0); PG8_MMA(1, 1, At, B1); PG8_BAR; PG8_SCHED;
;         }
;         if (wr == 0) PG8_BAR;
	s_setprio 1
	s_waitcnt lgkmcnt(6)
	v_mfma_f32_16x16x128_f8f6f4 v[158:161], v[26:33], v[180:187], v[158:161]
	v_mfma_f32_16x16x128_f8f6f4 v[154:157], v[18:25], v[180:187], v[154:157]
	s_waitcnt lgkmcnt(4)
	v_mfma_f32_16x16x128_f8f6f4 v[150:153], v[26:33], v[188:195], v[150:153]
	v_mfma_f32_16x16x128_f8f6f4 v[146:149], v[18:25], v[188:195], v[146:149]
	s_waitcnt lgkmcnt(2)
	v_mfma_f32_16x16x128_f8f6f4 v[142:145], v[26:33], v[196:203], v[142:145]
	v_mfma_f32_16x16x128_f8f6f4 v[138:141], v[18:25], v[196:203], v[138:141]
	s_waitcnt lgkmcnt(0)
	v_mfma_f32_16x16x128_f8f6f4 v[134:137], v[26:33], v[204:211], v[134:137]
	v_mfma_f32_16x16x128_f8f6f4 v[130:133], v[18:25], v[204:211], v[130:133]
	s_setprio 0
	s_setprio 1
	v_mfma_f32_16x16x128_f8f6f4 v[126:129], v[10:17], v[180:187], v[126:129]
	v_mfma_f32_16x16x128_f8f6f4 v[122:125], v[2:9], v[180:187], v[122:125]
	v_mfma_f32_16x16x128_f8f6f4 v[118:121], v[10:17], v[188:195], v[118:121]
	v_mfma_f32_16x16x128_f8f6f4 v[114:117], v[2:9], v[188:195], v[114:117]
	v_mfma_f32_16x16x128_f8f6f4 v[110:113], v[10:17], v[196:203], v[110:113]
	v_mfma_f32_16x16x128_f8f6f4 v[106:109], v[2:9], v[196:203], v[106:109]
	v_mfma_f32_16x16x128_f8f6f4 v[102:105], v[10:17], v[204:211], v[102:105]
	v_mfma_f32_16x16x128_f8f6f4 v[98:101], v[2:9], v[204:211], v[98:101]
	s_setprio 0
	s_barrier
	s_add_u32 s58, s24, 0x80
	s_addc_u32 s59, s25, 0
	s_add_u32 s60, s24, 0x20080
	s_addc_u32 s61, s25, 0
	ds_read_b128 v[180:183], v174 offset:49152
	ds_read_b128 v[184:187], v174 offset:50176
	ds_read_b128 v[188:191], v174 offset:51200
	ds_read_b128 v[192:195], v174 offset:52224
	ds_read_b128 v[196:199], v174 offset:53248
	ds_read_b128 v[200:203], v174 offset:54272
	ds_read_b128 v[204:207], v174 offset:55296
	ds_read_b128 v[208:211], v174 offset:56320
	s_mov_b32 s1, m0
	s_mov_b32 m0, s47
	s_nop 0
	global_load_lds_dwordx4 v166, s[58:59]
	s_mov_b32 m0, s48
	s_nop 0
	global_load_lds_dwordx4 v166, s[60:61]
	s_mov_b32 m0, s1
	s_add_u32 s58, s24, 0x40080
	s_addc_u32 s59, s25, 0
	s_add_u32 s24, s24, 0x60080
	s_addc_u32 s25, s25, 0
	s_mov_b32 s1, m0
	s_mov_b32 m0, s51
	s_nop 0
	global_load_lds_dwordx4 v166, s[58:59]
	s_mov_b32 m0, s52
	s_nop 0
	global_load_lds_dwordx4 v166, s[24:25]
	s_mov_b32 m0, s1
	s_add_u32 s24, s22, 0x80
	s_addc_u32 s25, s23, 0
	s_add_u32 s22, s22, 0x20080
	s_addc_u32 s23, s23, 0
	s_mov_b32 s1, m0
	s_mov_b32 m0, s49
	s_nop 0
	global_load_lds_dwordx4 v167, s[24:25]
	s_mov_b32 m0, s50
	s_nop 0
	global_load_lds_dwordx4 v167, s[22:23]
	s_mov_b32 m0, s1
	s_waitcnt vmcnt(8)
	s_waitcnt lgkmcnt(0)
	s_barrier
	s_setprio 1
	s_waitcnt lgkmcnt(6)
	v_mfma_f32_16x16x128_f8f6f4 v[94:97], v[26:33], v[180:187], v[94:97]
	v_mfma_f32_16x16x128_f8f6f4 v[90:93], v[18:25], v[180:187], v[90:93]
	s_waitcnt lgkmcnt(4)
	v_mfma_f32_16x16x128_f8f6f4 v[86:89], v[26:33], v[188:195], v[86:89]
	v_mfma_f32_16x16x128_f8f6f4 v[82:85], v[18:25], v[188:195], v[82:85]
	s_waitcnt lgkmcnt(2)
	v_mfma_f32_16x16x128_f8f6f4 v[78:81], v[26:33], v[196:203], v[78:81]
	v_mfma_f32_16x16x128_f8f6f4 v[74:77], v[18:25], v[196:203], v[74:77]
	s_waitcnt lgkmcnt(0)
	v_mfma_f32_16x16x128_f8f6f4 v[70:73], v[26:33], v[204:211], v[70:73]
	v_mfma_f32_16x16x128_f8f6f4 v[66:69], v[18:25], v[204:211], v[66:69]
	s_setprio 0
	s_setprio 1
	v_mfma_f32_16x16x128_f8f6f4 v[62:65], v[10:17], v[180:187], v[62:65]
	v_mfma_f32_16x16x128_f8f6f4 v[58:61], v[2:9], v[180:187], v[58:61]
	v_mfma_f32_16x16x128_f8f6f4 v[54:57], v[10:17], v[188:195], v[54:57]
	v_mfma_f32_16x16x128_f8f6f4 v[50:53], v[2:9], v[188:195], v[50:53]
	v_mfma_f32_16x16x128_f8f6f4 v[46:49], v[10:17], v[196:203], v[46:49]
	v_mfma_f32_16x16x128_f8f6f4 v[42:45], v[2:9], v[196:203], v[42:45]
	v_mfma_f32_16x16x128_f8f6f4 v[38:41], v[10:17], v[204:211], v[38:41]
	v_mfma_f32_16x16x128_f8f6f4 v[34:37], v[2:9], v[204:211], v[34:37]
	s_setprio 0
	s_barrier
	s_andn2_b64 vcc, exec, s[8:9]
	s_cbranch_vccnz .LBB0_878
	s_barrier

; __global__ void __launch_bounds__(NWAVES * 64, 2) fwd_kernel(Args args) {
;     extern __shared__ __attribute__((aligned(16))) unsigned char lds[];
	.amdhsa_kernel _Z10fwd_kernel4Args
		.amdhsa_group_segment_fixed_size 0
		.amdhsa_private_segment_fixed_size 0
		.amdhsa_kernarg_size 448
		.amdhsa_user_sgpr_count 2
		.amdhsa_user_sgpr_dispatch_ptr 0
		.amdhsa_user_sgpr_queue_ptr 0
		.amdhsa_user_sgpr_kernarg_segment_ptr 1
		.amdhsa_user_sgpr_dispatch_id 0
		.amdhsa_user_sgpr_kernarg_preload_length 0
		.amdhsa_user_sgpr_kernarg_preload_offset 0
		.amdhsa_user_sgpr_private_segment_size 0
		.amdhsa_uses_dynamic_stack 0
		.amdhsa_enable_private_segment 0
		.amdhsa_system_sgpr_workgroup_id_x 1
		.amdhsa_system_sgpr_workgroup_id_y 0
		.amdhsa_system_sgpr_workgroup_id_z 0
		.amdhsa_system_sgpr_workgroup_info 0
		.amdhsa_system_vgpr_workitem_id 0
		.amdhsa_next_free_vgpr 252
		.amdhsa_next_free_sgpr 100
		.amdhsa_accum_offset 252
		.amdhsa_reserve_vcc 1
		.amdhsa_float_round_mode_32 0
		.amdhsa_float_round_mode_16_64 0
		.amdhsa_float_denorm_mode_32 3
		.amdhsa_float_denorm_mode_16_64 3
		.amdhsa_dx10_clamp 1
		.amdhsa_ieee_mode 1
		.amdhsa_fp16_overflow 0
		.amdhsa_tg_split 0
		.amdhsa_exception_fp_ieee_invalid_op 0
		.amdhsa_exception_fp_denorm_src 0
		.amdhsa_exception_fp_ieee_div_zero 0
		.amdhsa_exception_fp_ieee_overflow 0
		.amdhsa_exception_fp_ieee_underflow 0
		.amdhsa_exception_fp_ieee_inexact 0
		.amdhsa_exception_int_div_zero 0
	.end_amdhsa_kernel

; __global__ void __launch_bounds__(NWAVES * 64, 2) fwd_kernel(Args args) {
;     extern __shared__ __attribute__((aligned(16))) unsigned char lds[];
amdhsa.kernels:
  - .agpr_count:     0
    .args:
      - .offset:         0
        .size:           192
        .value_kind:     by_value
      - .offset:         192
        .size:           4
        .value_kind:     hidden_block_count_x
      - .offset:         196
        .size:           4
        .value_kind:     hidden_block_count_y
      - .offset:         200
        .size:           4
        .value_kind:     hidden_block_count_z
      - .offset:         204
        .size:           2
        .value_kind:     hidden_group_size_x
      - .offset:         206
        .size:           2
        .value_kind:     hidden_group_size_y
      - .offset:         208
        .size:           2
        .value_kind:     hidden_group_size_z
      - .offset:         210
        .size:           2
        .value_kind:     hidden_remainder_x
      - .offset:         212
        .size:           2
        .value_kind:     hidden_remainder_y
      - .offset:         214
        .size:           2
        .value_kind:     hidden_remainder_z
      - .offset:         232
        .size:           8
        .value_kind:     hidden_global_offset_x
      - .offset:         240
        .size:           8
        .value_kind:     hidden_global_offset_y
      - .offset:         248
        .size:           8
        .value_kind:     hidden_global_offset_z
      - .offset:         256
        .size:           2
        .value_kind:     hidden_grid_dims
      - .offset:         312
        .size:           4
        .value_kind:     hidden_dynamic_lds_size
    .group_segment_fixed_size: 0
    .kernarg_segment_align: 8
    .kernarg_segment_size: 448
    .language:       OpenCL C
    .language_version:
      - 2
      - 0
    .max_flat_workgroup_size: 512
    .name:           _Z10fwd_kernel4Args
    .private_segment_fixed_size: 0
    .sgpr_count:     106
    .sgpr_spill_count: 108
    .symbol:         _Z10fwd_kernel4Args.kd
    .uniform_work_group_size: 1
    .uses_dynamic_stack: false
    .vgpr_count:     252
    .vgpr_spill_count: 0
    .wavefront_size: 64
